# GEMM tiles: first K-loop iteration peeled with SrcC = 0 in its first product per accumulator, the 128 zeroing moves per tile removed (fp8 GEMMs of P1, P7, P10, P11)
# speedup vs baseline: 1.0418x; 1.0081x over previous
;     __device__ __forceinline__ bool next(int i, Unit& u) const { u.aux = 0; return t.map(i, u.pm, u.pn); }
;     __device__ __forceinline__ bool next(int i, Unit& u) const { u.aux = i & 1; return t.map(i >> 1, u.pm, u.pn); }
; #define PG8_WAIT_V(n) asm volatile("s_waitcnt vmcnt(" #n ")" ::: "memory")
; #define PG8_BAR __builtin_amdgcn_s_barrier()
; template <class Epi, class Sched, bool ALIGN_EPI, bool F8 = false, int F8SC = F8_SCALES>
; __device__ __forceinline__ void gemm_phase(PG8_LAS unsigned char* lds, const __amdgpu_buffer_rsrc_t rsrc, const int lda, const int ldb, const int K, const Sched& S, const Epi& E) {
;     ...
;     Unit cur, nxt; int ui = 0;
;     if (!S.next(0, cur)) return;
;     f32x4 acc[2][2][4][2];
;     PG8_ZERO();
;     i32x8 At[4], B0[2], B1[2];
;     unsigned cA, cB; S.bases(cur, cA, cB); cA = __builtin_amdgcn_readfirstlane(cA); cB = __builtin_amdgcn_readfirstlane(cB);
;     PG8_STAGE(PG8_SB(0, 0), cB, voffB); PG8_STAGE(PG8_SB(0, 1), cB + hsB, voffB); PG8_STAGE(PG8_SA(0, 0), cA, voffA); PG8_STAGE(PG8_SA(0, 1), cA + hsA, voffA);
;     if (wr == 1) PG8_BAR;
;     PG8_WAIT_V(2); PG8_BAR;
;     PG8_STAGE(PG8_SB(1, 0), cB + kstep, voffB); PG8_STAGE(PG8_SA(1, 0), cA + kstep, voffA); PG8_STAGE(PG8_SB(1, 1), cB + hsB + kstep, voffB);
;     PG8_WAIT_V(6); PG8_BAR;
;     for (;;) {
;         const bool has_next = S.next(ui + 1, nxt);
;         unsigned nA = cA, nB = cB; if (has_next) { S.bases(nxt, nA, nB); nA = __builtin_amdgcn_readfirstlane(nA); nB = __builtin_amdgcn_readfirstlane(nB); }
; #pragma unroll 1
;         for (int t = 0; t < nt; t += 2) {
;             const bool last = (t == nt - 2);
;             const unsigned a1 = cA + (unsigned)(t + 1) * kstep;
;             const unsigned a2 = last ? nA : cA + (unsigned)(t + 2) * kstep, b2 = last ? nB : cB + (unsigned)(t + 2) * kstep;
;             const unsigned a3 = a2 + kstep, b3 = b2 + kstep;
;             PG8_LDB(B0, 0, 0); PG8_LDB(B1, 0, 1); PG8_SCHED; PG8_LDA(At, 0, 0); PG8_STAGE(PG8_SA(1, 1), a1 + hsA, voffA);
;             PG8_WAIT_V(8); PG8_WAIT_L(0); PG8_BAR; PG8_MMA(0, 0, At, B0); PG8_MMA(0, 1, At, B1); PG8_BAR; PG8_SCHED;
;             PG8_LDA(At, 0, 1); PG8_STAGE(PG8_SB(0, 0), b2, voffB); PG8_STAGE(PG8_SB(0, 1), b2 + hsB, voffB); PG8_STAGE(PG8_SA(0, 0), a2, voffA);
;             PG8_WAIT_V(8); PG8_WAIT_L(0); PG8_BAR; PG8_MMA(1, 0, At, B0); PG8_MMA(1, 1, At, B1); PG8_BAR; PG8_SCHED;
.LBB0_126:
	s_add_i32 s0, s7, 0x60080
	s_add_i32 s1, s6, 0x100
	s_mov_b32 s6, -2
	ds_read_b128 v[158:161], v151
	ds_read_b128 v[162:165], v151 offset:1024
	ds_read_b128 v[166:169], v151 offset:2048
	ds_read_b128 v[170:173], v151 offset:3072
	ds_read_b128 v[174:177], v152
	ds_read_b128 v[178:181], v152 offset:1024
	ds_read_b128 v[182:185], v152 offset:2048
	ds_read_b128 v[186:189], v152 offset:3072
	s_add_i32 s7, s0, 0xfffa0080
	s_cmp_eq_u32 s6, 12
	s_cselect_b32 s7, s59, s7
	s_cselect_b32 s9, s60, s1
	s_add_i32 s8, s7, 0x80
	s_add_i32 s10, s0, 0xfffe0000
	s_mov_b32 s80, s96
	s_mov_b32 m0, s53
	ds_read_b128 v[190:193], v153
	ds_read_b128 v[194:197], v153 offset:1024
	ds_read_b128 v[198:201], v153 offset:2048
	ds_read_b128 v[202:205], v153 offset:3072
	ds_read_b128 v[206:209], v153 offset:4096
	ds_read_b128 v[210:213], v153 offset:5120
	ds_read_b128 v[214:217], v153 offset:6144
	ds_read_b128 v[218:221], v153 offset:7168
	buffer_load_dwordx4 v1, s[80:83], s10 offen lds
	s_mov_b32 m0, s54
	s_nop 0
	buffer_load_dwordx4 v1, s[80:83], s0 offen lds
	s_waitcnt vmcnt(8)
	s_waitcnt lgkmcnt(0)
	s_barrier
	s_setprio 1
	s_waitcnt lgkmcnt(4)
	v_mfma_scale_f32_16x16x128_f8f6f4 v[126:129], v[158:165], v[198:205], 0, v154, v154 op_sel:[0,1,0] op_sel_hi:[0,0,0]
	v_mfma_scale_f32_16x16x128_f8f6f4 v[122:125], v[166:173], v[198:205], 0, v154, v154 op_sel:[0,1,0] op_sel_hi:[0,0,0]
	s_waitcnt lgkmcnt(2)
	v_mfma_scale_f32_16x16x128_f8f6f4 v[118:121], v[158:165], v[206:213], 0, v154, v154 op_sel:[0,1,0] op_sel_hi:[0,0,0]
	v_mfma_scale_f32_16x16x128_f8f6f4 v[114:117], v[166:173], v[206:213], 0, v154, v154 op_sel:[0,1,0] op_sel_hi:[0,0,0]
	s_waitcnt lgkmcnt(0)
	v_mfma_scale_f32_16x16x128_f8f6f4 v[110:113], v[158:165], v[214:221], 0, v154, v154 op_sel:[0,1,0] op_sel_hi:[0,0,0]
	v_mfma_scale_f32_16x16x128_f8f6f4 v[106:109], v[166:173], v[214:221], 0, v154, v154 op_sel:[0,1,0] op_sel_hi:[0,0,0]
	v_mfma_scale_f32_16x16x128_f8f6f4 v[94:97], v[158:165], v[190:197], 0, v154, v154 op_sel:[0,1,0] op_sel_hi:[0,0,0]
	v_mfma_scale_f32_16x16x128_f8f6f4 v[102:105], v[166:173], v[190:197], 0, v154, v154 op_sel:[0,1,0] op_sel_hi:[0,0,0]
	s_setprio 0
	s_setprio 1
	v_mfma_scale_f32_16x16x128_f8f6f4 v[144:147], v[174:181], v[190:197], 0, v154, v154 op_sel:[0,1,0] op_sel_hi:[0,0,0]
	v_mfma_scale_f32_16x16x128_f8f6f4 v[190:193], v[182:189], v[190:197], 0, v154, v154 op_sel:[0,1,0] op_sel_hi:[0,0,0]
	v_mfma_scale_f32_16x16x128_f8f6f4 v[194:197], v[174:181], v[198:205], 0, v154, v154 op_sel:[0,1,0] op_sel_hi:[0,0,0]
	v_mfma_scale_f32_16x16x128_f8f6f4 v[198:201], v[182:189], v[198:205], 0, v154, v154 op_sel:[0,1,0] op_sel_hi:[0,0,0]
	v_mfma_scale_f32_16x16x128_f8f6f4 v[202:205], v[174:181], v[206:213], 0, v154, v154 op_sel:[0,1,0] op_sel_hi:[0,0,0]
	v_mfma_scale_f32_16x16x128_f8f6f4 v[206:209], v[182:189], v[206:213], 0, v154, v154 op_sel:[0,1,0] op_sel_hi:[0,0,0]
	v_mfma_scale_f32_16x16x128_f8f6f4 v[210:213], v[174:181], v[214:221], 0, v154, v154 op_sel:[0,1,0] op_sel_hi:[0,0,0]
	v_mfma_scale_f32_16x16x128_f8f6f4 v[214:217], v[182:189], v[214:221], 0, v154, v154 op_sel:[0,1,0] op_sel_hi:[0,0,0]
	s_setprio 0
	s_barrier
	s_mov_b32 m0, s34
	s_nop 3
	ds_read_b128 v[34:37], v153 offset:16384
	ds_read_b128 v[38:41], v153 offset:17408
	ds_read_b128 v[42:45], v153 offset:18432
	ds_read_b128 v[46:49], v153 offset:19456
	ds_read_b128 v[50:53], v153 offset:20480
	ds_read_b128 v[54:57], v153 offset:21504
	ds_read_b128 v[58:61], v153 offset:22528
	ds_read_b128 v[62:65], v153 offset:23552
	buffer_load_dwordx4 v150, s[80:83], s9 offen lds
	s_add_i32 s10, s9, 0x20000
	s_mov_b32 m0, s35
	s_nop 0
	buffer_load_dwordx4 v150, s[80:83], s10 offen lds
	s_add_i32 s10, s9, 0x40000
	s_mov_b32 m0, s36
	s_nop 0
	buffer_load_dwordx4 v150, s[80:83], s10 offen lds
	s_add_i32 s10, s9, 0x60000
	s_mov_b32 m0, s37
	s_nop 0
	buffer_load_dwordx4 v150, s[80:83], s10 offen lds
	s_mov_b32 m0, s13
	s_add_i32 s10, s7, 0x20000
	buffer_load_dwordx4 v1, s[80:83], s7 offen lds
	s_mov_b32 m0, s38
	s_nop 0
	buffer_load_dwordx4 v1, s[80:83], s10 offen lds
	s_waitcnt vmcnt(8)
	s_waitcnt lgkmcnt(0)
	s_barrier
	s_setprio 1
	s_waitcnt lgkmcnt(6)
	v_mfma_scale_f32_16x16x128_f8f6f4 v[98:101], v[158:165], v[34:41], 0, v154, v154 op_sel:[0,1,0] op_sel_hi:[0,0,0]
	v_mfma_scale_f32_16x16x128_f8f6f4 v[90:93], v[166:173], v[34:41], 0, v154, v154 op_sel:[0,1,0] op_sel_hi:[0,0,0]
	s_waitcnt lgkmcnt(4)
	v_mfma_scale_f32_16x16x128_f8f6f4 v[86:89], v[158:165], v[42:49], 0, v154, v154 op_sel:[0,1,0] op_sel_hi:[0,0,0]
	v_mfma_scale_f32_16x16x128_f8f6f4 v[82:85], v[166:173], v[42:49], 0, v154, v154 op_sel:[0,1,0] op_sel_hi:[0,0,0]
	s_waitcnt lgkmcnt(2)
	v_mfma_scale_f32_16x16x128_f8f6f4 v[78:81], v[158:165], v[50:57], 0, v154, v154 op_sel:[0,1,0] op_sel_hi:[0,0,0]
	v_mfma_scale_f32_16x16x128_f8f6f4 v[74:77], v[166:173], v[50:57], 0, v154, v154 op_sel:[0,1,0] op_sel_hi:[0,0,0]
	s_waitcnt lgkmcnt(0)
	v_mfma_scale_f32_16x16x128_f8f6f4 v[218:221], v[158:165], v[58:65], 0, v154, v154 op_sel:[0,1,0] op_sel_hi:[0,0,0]
	v_mfma_scale_f32_16x16x128_f8f6f4 v[222:225], v[166:173], v[58:65], 0, v154, v154 op_sel:[0,1,0] op_sel_hi:[0,0,0]
	s_setprio 0
	s_setprio 1
	v_mfma_scale_f32_16x16x128_f8f6f4 v[226:229], v[174:181], v[34:41], 0, v154, v154 op_sel:[0,1,0] op_sel_hi:[0,0,0]
	v_mfma_scale_f32_16x16x128_f8f6f4 v[230:233], v[182:189], v[34:41], 0, v154, v154 op_sel:[0,1,0] op_sel_hi:[0,0,0]
	v_mfma_scale_f32_16x16x128_f8f6f4 v[234:237], v[174:181], v[42:49], 0, v154, v154 op_sel:[0,1,0] op_sel_hi:[0,0,0]
	v_mfma_scale_f32_16x16x128_f8f6f4 v[238:241], v[182:189], v[42:49], 0, v154, v154 op_sel:[0,1,0] op_sel_hi:[0,0,0]
	v_mfma_scale_f32_16x16x128_f8f6f4 v[242:245], v[174:181], v[50:57], 0, v154, v154 op_sel:[0,1,0] op_sel_hi:[0,0,0]
	v_mfma_scale_f32_16x16x128_f8f6f4 v[246:249], v[182:189], v[50:57], 0, v154, v154 op_sel:[0,1,0] op_sel_hi:[0,0,0]
	v_mfma_scale_f32_16x16x128_f8f6f4 v[250:253], v[174:181], v[58:65], 0, v154, v154 op_sel:[0,1,0] op_sel_hi:[0,0,0]
	v_mfma_scale_f32_16x16x128_f8f6f4 v[138:141], v[182:189], v[58:65], 0, v154, v154 op_sel:[0,1,0] op_sel_hi:[0,0,0]
	s_setprio 0
	s_barrier
; #define PG8_STAGE(bufoff, goff, voff) do { _Pragma("unroll") for (int _i = 0; _i < 2; ++_i) \
;         __builtin_amdgcn_raw_ptr_buffer_load_lds(rsrc, (PG8_LAS void*)(lds + (bufoff) + ldsw + _i * 8192), 16, (int)(voff), (int)((goff) + _i * p1##voff), 0, 0); } while (0)
; #define PG8_LDA(dst, b, h) do { _Pragma("unroll") for (int m = 0; m < 4; ++m) dst[m] = PG8_LD8(lds + PG8_SA(b, h) + aoff + m * 2048); } while (0)
; #define PG8_LDB(dst, b, h) do { _Pragma("unroll") for (int n = 0; n < 2; ++n) dst[n] = PG8_LD8(lds + PG8_SB(b, h) + boff + n * 2048); } while (0)
; #define PG8_WAIT_V(n) asm volatile("s_waitcnt vmcnt(" #n ")" ::: "memory")
; #define PG8_WAIT_L(n) asm volatile("s_waitcnt lgkmcnt(" #n ")" ::: "memory")
; #define PG8_BAR __builtin_amdgcn_s_barrier()
; #define PG8_SCHED __builtin_amdgcn_sched_barrier(0)
; template <class Epi, class Sched, bool ALIGN_EPI, bool F8 = false, int F8SC = F8_SCALES>
; __device__ __forceinline__ void gemm_phase(PG8_LAS unsigned char* lds, const __amdgpu_buffer_rsrc_t rsrc, const int lda, const int ldb, const int K, const Sched& S, const Epi& E) {
;     ...
;             PG8_LDB(B0, 1, 0); PG8_LDB(B1, 1, 1); PG8_SCHED; PG8_LDA(At, 1, 0); PG8_STAGE(PG8_SA(0, 1), a2 + hsA, voffA);
;             PG8_WAIT_V(8); PG8_WAIT_L(0); PG8_BAR; PG8_MMA(0, 0, At, B0); PG8_MMA(0, 1, At, B1); PG8_BAR; PG8_SCHED;
;             PG8_LDA(At, 1, 1); PG8_STAGE(PG8_SB(1, 0), b3, voffB); PG8_STAGE(PG8_SB(1, 1), b3 + hsB, voffB); PG8_STAGE(PG8_SA(1, 0), a3, voffA);
;             PG8_WAIT_V(8); PG8_WAIT_L(0); PG8_BAR; PG8_MMA(1, 0, At, B0); PG8_MMA(1, 1, At, B1); PG8_BAR; PG8_SCHED;
;         }
	s_nop 4
	ds_read_b128 v[2:5], v155
	ds_read_b128 v[6:9], v155 offset:1024
	ds_read_b128 v[10:13], v155 offset:2048
	ds_read_b128 v[14:17], v155 offset:3072
	ds_read_b128 v[158:161], v156
	ds_read_b128 v[162:165], v156 offset:1024
	ds_read_b128 v[166:169], v156 offset:2048
	ds_read_b128 v[170:173], v156 offset:3072
	s_mov_b32 m0, s39
	s_add_i32 s10, s7, 0x40000
	ds_read_b128 v[18:21], v153 offset:32768
	ds_read_b128 v[22:25], v153 offset:33792
	ds_read_b128 v[26:29], v153 offset:34816
	ds_read_b128 v[30:33], v153 offset:35840
	ds_read_b128 v[34:37], v153 offset:36864
	ds_read_b128 v[38:41], v153 offset:37888
	ds_read_b128 v[66:69], v153 offset:38912
	ds_read_b128 v[70:73], v153 offset:39936
	buffer_load_dwordx4 v1, s[80:83], s10 offen lds
	s_add_i32 s10, s7, 0x60000
	s_mov_b32 m0, s40
	s_nop 0
	buffer_load_dwordx4 v1, s[80:83], s10 offen lds
	s_waitcnt vmcnt(8)
	s_waitcnt lgkmcnt(0)
	s_barrier
	s_setprio 1
	s_waitcnt lgkmcnt(6)
	v_mfma_scale_f32_16x16x128_f8f6f4 v[134:137], v[2:9], v[18:25], v[94:97], v154, v154 op_sel:[0,1,0] op_sel_hi:[0,0,0]
	v_mfma_scale_f32_16x16x128_f8f6f4 v[130:133], v[10:17], v[18:25], v[102:105], v154, v154 op_sel:[0,1,0] op_sel_hi:[0,0,0]
	s_waitcnt lgkmcnt(4)
	v_mfma_scale_f32_16x16x128_f8f6f4 v[126:129], v[2:9], v[26:33], v[126:129], v154, v154 op_sel:[0,1,0] op_sel_hi:[0,0,0]
	v_mfma_scale_f32_16x16x128_f8f6f4 v[122:125], v[10:17], v[26:33], v[122:125], v154, v154 op_sel:[0,1,0] op_sel_hi:[0,0,0]
	s_waitcnt lgkmcnt(2)
	v_mfma_scale_f32_16x16x128_f8f6f4 v[118:121], v[2:9], v[34:41], v[118:121], v154, v154 op_sel:[0,1,0] op_sel_hi:[0,0,0]
	v_mfma_scale_f32_16x16x128_f8f6f4 v[114:117], v[10:17], v[34:41], v[114:117], v154, v154 op_sel:[0,1,0] op_sel_hi:[0,0,0]
	s_waitcnt lgkmcnt(0)
	v_mfma_scale_f32_16x16x128_f8f6f4 v[110:113], v[2:9], v[66:73], v[110:113], v154, v154 op_sel:[0,1,0] op_sel_hi:[0,0,0]
	v_mfma_scale_f32_16x16x128_f8f6f4 v[106:109], v[10:17], v[66:73], v[106:109], v154, v154 op_sel:[0,1,0] op_sel_hi:[0,0,0]
	s_setprio 0
	s_setprio 1
	v_mfma_scale_f32_16x16x128_f8f6f4 v[62:65], v[158:165], v[18:25], v[144:147], v154, v154 op_sel:[0,1,0] op_sel_hi:[0,0,0]
	v_mfma_scale_f32_16x16x128_f8f6f4 v[58:61], v[166:173], v[18:25], v[190:193], v154, v154 op_sel:[0,1,0] op_sel_hi:[0,0,0]
	v_mfma_scale_f32_16x16x128_f8f6f4 v[54:57], v[158:165], v[26:33], v[194:197], v154, v154 op_sel:[0,1,0] op_sel_hi:[0,0,0]
	v_mfma_scale_f32_16x16x128_f8f6f4 v[50:53], v[166:173], v[26:33], v[198:201], v154, v154 op_sel:[0,1,0] op_sel_hi:[0,0,0]
	v_mfma_scale_f32_16x16x128_f8f6f4 v[46:49], v[158:165], v[34:41], v[202:205], v154, v154 op_sel:[0,1,0] op_sel_hi:[0,0,0]
	v_mfma_scale_f32_16x16x128_f8f6f4 v[42:45], v[166:173], v[34:41], v[206:209], v154, v154 op_sel:[0,1,0] op_sel_hi:[0,0,0]
	v_mfma_scale_f32_16x16x128_f8f6f4 v[38:41], v[158:165], v[66:73], v[210:213], v154, v154 op_sel:[0,1,0] op_sel_hi:[0,0,0]
	v_mfma_scale_f32_16x16x128_f8f6f4 v[34:37], v[166:173], v[66:73], v[214:217], v154, v154 op_sel:[0,1,0] op_sel_hi:[0,0,0]
	s_setprio 0
	s_barrier
	s_mov_b32 m0, s46
	s_add_i32 s10, s9, 0x80
	ds_read_b128 v[18:21], v153 offset:49152
	ds_read_b128 v[22:25], v153 offset:50176
	ds_read_b128 v[174:177], v153 offset:51200
	ds_read_b128 v[178:181], v153 offset:52224
	ds_read_b128 v[182:185], v153 offset:53248
	ds_read_b128 v[186:189], v153 offset:54272
	ds_read_b128 v[190:193], v153 offset:55296
	ds_read_b128 v[194:197], v153 offset:56320
	buffer_load_dwordx4 v150, s[80:83], s10 offen lds
	s_add_i32 s10, s9, 0x20080
	s_mov_b32 m0, s47
	s_add_i32 s7, s7, 0x20080
	buffer_load_dwordx4 v150, s[80:83], s10 offen lds
	s_add_i32 s10, s9, 0x40080
	s_mov_b32 m0, s50
	s_add_i32 s9, s9, 0x60080
	buffer_load_dwordx4 v150, s[80:83], s10 offen lds
	s_mov_b32 m0, s51
	s_nop 0
	buffer_load_dwordx4 v150, s[80:83], s9 offen lds
	s_mov_b32 m0, s48
	s_nop 0
	buffer_load_dwordx4 v1, s[80:83], s8 offen lds
	s_mov_b32 m0, s49
	s_nop 0
	buffer_load_dwordx4 v1, s[80:83], s7 offen lds
	s_waitcnt vmcnt(8)
	s_waitcnt lgkmcnt(0)
	s_barrier
	s_setprio 1
	s_waitcnt lgkmcnt(6)
	v_mfma_scale_f32_16x16x128_f8f6f4 v[98:101], v[2:9], v[18:25], v[98:101], v154, v154 op_sel:[0,1,0] op_sel_hi:[0,0,0]
	v_mfma_scale_f32_16x16x128_f8f6f4 v[90:93], v[10:17], v[18:25], v[90:93], v154, v154 op_sel:[0,1,0] op_sel_hi:[0,0,0]
	s_waitcnt lgkmcnt(4)
	v_mfma_scale_f32_16x16x128_f8f6f4 v[86:89], v[2:9], v[174:181], v[86:89], v154, v154 op_sel:[0,1,0] op_sel_hi:[0,0,0]
	v_mfma_scale_f32_16x16x128_f8f6f4 v[82:85], v[10:17], v[174:181], v[82:85], v154, v154 op_sel:[0,1,0] op_sel_hi:[0,0,0]
	s_waitcnt lgkmcnt(2)
	v_mfma_scale_f32_16x16x128_f8f6f4 v[78:81], v[2:9], v[182:189], v[78:81], v154, v154 op_sel:[0,1,0] op_sel_hi:[0,0,0]
	v_mfma_scale_f32_16x16x128_f8f6f4 v[74:77], v[10:17], v[182:189], v[74:77], v154, v154 op_sel:[0,1,0] op_sel_hi:[0,0,0]
	s_waitcnt lgkmcnt(0)
	v_mfma_scale_f32_16x16x128_f8f6f4 v[70:73], v[2:9], v[190:197], v[218:221], v154, v154 op_sel:[0,1,0] op_sel_hi:[0,0,0]
	v_mfma_scale_f32_16x16x128_f8f6f4 v[66:69], v[10:17], v[190:197], v[222:225], v154, v154 op_sel:[0,1,0] op_sel_hi:[0,0,0]
	s_setprio 0
	s_setprio 1
	v_mfma_scale_f32_16x16x128_f8f6f4 v[30:33], v[158:165], v[18:25], v[226:229], v154, v154 op_sel:[0,1,0] op_sel_hi:[0,0,0]
	v_mfma_scale_f32_16x16x128_f8f6f4 v[26:29], v[166:173], v[18:25], v[230:233], v154, v154 op_sel:[0,1,0] op_sel_hi:[0,0,0]
	v_mfma_scale_f32_16x16x128_f8f6f4 v[22:25], v[158:165], v[174:181], v[234:237], v154, v154 op_sel:[0,1,0] op_sel_hi:[0,0,0]
	v_mfma_scale_f32_16x16x128_f8f6f4 v[18:21], v[166:173], v[174:181], v[238:241], v154, v154 op_sel:[0,1,0] op_sel_hi:[0,0,0]
	v_mfma_scale_f32_16x16x128_f8f6f4 v[14:17], v[158:165], v[182:189], v[242:245], v154, v154 op_sel:[0,1,0] op_sel_hi:[0,0,0]
	v_mfma_scale_f32_16x16x128_f8f6f4 v[10:13], v[166:173], v[182:189], v[246:249], v154, v154 op_sel:[0,1,0] op_sel_hi:[0,0,0]
	v_mfma_scale_f32_16x16x128_f8f6f4 v[6:9], v[158:165], v[190:197], v[250:253], v154, v154 op_sel:[0,1,0] op_sel_hi:[0,0,0]
	v_mfma_scale_f32_16x16x128_f8f6f4 v[2:5], v[166:173], v[190:197], v[138:141], v154, v154 op_sel:[0,1,0] op_sel_hi:[0,0,0]
	s_setprio 0
	s_barrier
	s_add_i32 s6, s6, 2
	s_addk_i32 s0, 0x100
	s_addk_i32 s1, 0x100
	s_cmp_gt_u32 s6, 13
	s_cbranch_scc0 .LBB0_127
	s_branch .Lpeel_after_127

; #define PG8_BAR __builtin_amdgcn_s_barrier()
; template <class Epi, class Sched, bool ALIGN_EPI, bool F8 = false, int F8SC = F8_SCALES>
; __device__ __forceinline__ void gemm_phase(PG8_LAS unsigned char* lds, const __amdgpu_buffer_rsrc_t rsrc, const int lda, const int ldb, const int K, const Sched& S, const Epi& E) {
;     ...
;         if constexpr (ALIGN_EPI) { if (wr == 0) PG8_BAR; }
.Lpeel_after_127:
	s_and_b64 vcc, exec, s[88:89]
	s_cbranch_vccz .LBB0_130
	s_barrier

;     __device__ __forceinline__ bool next(int i, Unit& u) const { u.aux = 0; return t.map(i, u.pm, u.pn); }
;     __device__ __forceinline__ bool next(int i, Unit& u) const { u.aux = i & 1; return t.map(i >> 1, u.pm, u.pn); }
; #define PG8_WAIT_V(n) asm volatile("s_waitcnt vmcnt(" #n ")" ::: "memory")
; #define PG8_BAR __builtin_amdgcn_s_barrier()
; template <class Epi, class Sched, bool ALIGN_EPI, bool F8 = false, int F8SC = F8_SCALES>
; __device__ __forceinline__ void gemm_phase(PG8_LAS unsigned char* lds, const __amdgpu_buffer_rsrc_t rsrc, const int lda, const int ldb, const int K, const Sched& S, const Epi& E) {
;     ...
;     Unit cur, nxt; int ui = 0;
;     if (!S.next(0, cur)) return;
;     f32x4 acc[2][2][4][2];
;     PG8_ZERO();
;     i32x8 At[4], B0[2], B1[2];
;     unsigned cA, cB; S.bases(cur, cA, cB); cA = __builtin_amdgcn_readfirstlane(cA); cB = __builtin_amdgcn_readfirstlane(cB);
;     PG8_STAGE(PG8_SB(0, 0), cB, voffB); PG8_STAGE(PG8_SB(0, 1), cB + hsB, voffB); PG8_STAGE(PG8_SA(0, 0), cA, voffA); PG8_STAGE(PG8_SA(0, 1), cA + hsA, voffA);
;     if (wr == 1) PG8_BAR;
;     PG8_WAIT_V(2); PG8_BAR;
;     PG8_STAGE(PG8_SB(1, 0), cB + kstep, voffB); PG8_STAGE(PG8_SA(1, 0), cA + kstep, voffA); PG8_STAGE(PG8_SB(1, 1), cB + hsB + kstep, voffB);
;     PG8_WAIT_V(6); PG8_BAR;
;     for (;;) {
;         const bool has_next = S.next(ui + 1, nxt);
;         unsigned nA = cA, nB = cB; if (has_next) { S.bases(nxt, nA, nB); nA = __builtin_amdgcn_readfirstlane(nA); nB = __builtin_amdgcn_readfirstlane(nB); }
; #pragma unroll 1
;         for (int t = 0; t < nt; t += 2) {
;             const bool last = (t == nt - 2);
;             const unsigned a1 = cA + (unsigned)(t + 1) * kstep;
;             const unsigned a2 = last ? nA : cA + (unsigned)(t + 2) * kstep, b2 = last ? nB : cB + (unsigned)(t + 2) * kstep;
;             const unsigned a3 = a2 + kstep, b3 = b2 + kstep;
;             PG8_LDB(B0, 0, 0); PG8_LDB(B1, 0, 1); PG8_SCHED; PG8_LDA(At, 0, 0); PG8_STAGE(PG8_SA(1, 1), a1 + hsA, voffA);
;             PG8_WAIT_V(8); PG8_WAIT_L(0); PG8_BAR; PG8_MMA(0, 0, At, B0); PG8_MMA(0, 1, At, B1); PG8_BAR; PG8_SCHED;
;             PG8_LDA(At, 0, 1); PG8_STAGE(PG8_SB(0, 0), b2, voffB); PG8_STAGE(PG8_SB(0, 1), b2 + hsB, voffB); PG8_STAGE(PG8_SA(0, 0), a2, voffA);
;             PG8_WAIT_V(8); PG8_WAIT_L(0); PG8_BAR; PG8_MMA(1, 0, At, B0); PG8_MMA(1, 1, At, B1); PG8_BAR; PG8_SCHED;
.LBB0_738:
	s_add_i32 s36, s36, 0x60080
	s_addk_i32 s37, 0x100
	s_mov_b32 s38, -2
	ds_read_b128 v[148:151], v140
	ds_read_b128 v[152:155], v140 offset:1024
	ds_read_b128 v[156:159], v140 offset:2048
	ds_read_b128 v[160:163], v140 offset:3072
	ds_read_b128 v[164:167], v141
	ds_read_b128 v[168:171], v141 offset:1024
	ds_read_b128 v[172:175], v141 offset:2048
	ds_read_b128 v[176:179], v141 offset:3072
	s_add_i32 s39, s36, 0xfffa0080
	s_cmp_eq_u32 s38, 12
	s_cselect_b32 s39, s4, s39
	s_cselect_b32 s41, s5, s37
	s_add_i32 s40, s39, 0x80
	s_add_i32 s42, s36, 0xfffe0000
	s_mov_b32 s80, s96
	s_mov_b32 m0, s27
	ds_read_b128 v[180:183], v142
	ds_read_b128 v[184:187], v142 offset:1024
	ds_read_b128 v[188:191], v142 offset:2048
	ds_read_b128 v[192:195], v142 offset:3072
	ds_read_b128 v[196:199], v142 offset:4096
	ds_read_b128 v[200:203], v142 offset:5120
	ds_read_b128 v[204:207], v142 offset:6144
	ds_read_b128 v[208:211], v142 offset:7168
	buffer_load_dwordx4 v1, s[80:83], s42 offen lds
	s_mov_b32 m0, s28
	s_nop 0
	buffer_load_dwordx4 v1, s[80:83], s36 offen lds
	s_waitcnt vmcnt(8)
	s_waitcnt lgkmcnt(0)
	s_barrier
	s_setprio 1
	s_waitcnt lgkmcnt(6)
	v_mfma_scale_f32_16x16x128_f8f6f4 v[126:129], v[148:155], v[180:187], 0, v143, v143 op_sel:[0,1,0] op_sel_hi:[0,0,0]
	v_mfma_scale_f32_16x16x128_f8f6f4 v[122:125], v[156:163], v[180:187], 0, v143, v143 op_sel:[0,1,0] op_sel_hi:[0,0,0]
	s_waitcnt lgkmcnt(4)
	v_mfma_scale_f32_16x16x128_f8f6f4 v[118:121], v[148:155], v[188:195], 0, v143, v143 op_sel:[0,1,0] op_sel_hi:[0,0,0]
	v_mfma_scale_f32_16x16x128_f8f6f4 v[110:113], v[156:163], v[188:195], 0, v143, v143 op_sel:[0,1,0] op_sel_hi:[0,0,0]
	s_waitcnt lgkmcnt(2)
	v_mfma_scale_f32_16x16x128_f8f6f4 v[102:105], v[148:155], v[196:203], 0, v143, v143 op_sel:[0,1,0] op_sel_hi:[0,0,0]
	v_mfma_scale_f32_16x16x128_f8f6f4 v[136:139], v[156:163], v[196:203], 0, v143, v143 op_sel:[0,1,0] op_sel_hi:[0,0,0]
	s_waitcnt lgkmcnt(0)
	v_mfma_scale_f32_16x16x128_f8f6f4 v[212:215], v[148:155], v[204:211], 0, v143, v143 op_sel:[0,1,0] op_sel_hi:[0,0,0]
	v_mfma_scale_f32_16x16x128_f8f6f4 v[216:219], v[156:163], v[204:211], 0, v143, v143 op_sel:[0,1,0] op_sel_hi:[0,0,0]
	s_setprio 0
	s_setprio 1
	v_mfma_scale_f32_16x16x128_f8f6f4 v[114:117], v[164:171], v[180:187], 0, v143, v143 op_sel:[0,1,0] op_sel_hi:[0,0,0]
	v_mfma_scale_f32_16x16x128_f8f6f4 v[106:109], v[172:179], v[180:187], 0, v143, v143 op_sel:[0,1,0] op_sel_hi:[0,0,0]
	v_mfma_scale_f32_16x16x128_f8f6f4 v[98:101], v[164:171], v[188:195], 0, v143, v143 op_sel:[0,1,0] op_sel_hi:[0,0,0]
	v_mfma_scale_f32_16x16x128_f8f6f4 v[180:183], v[172:179], v[188:195], 0, v143, v143 op_sel:[0,1,0] op_sel_hi:[0,0,0]
	v_mfma_scale_f32_16x16x128_f8f6f4 v[184:187], v[164:171], v[196:203], 0, v143, v143 op_sel:[0,1,0] op_sel_hi:[0,0,0]
	v_mfma_scale_f32_16x16x128_f8f6f4 v[188:191], v[172:179], v[196:203], 0, v143, v143 op_sel:[0,1,0] op_sel_hi:[0,0,0]
	v_mfma_scale_f32_16x16x128_f8f6f4 v[192:195], v[164:171], v[204:211], 0, v143, v143 op_sel:[0,1,0] op_sel_hi:[0,0,0]
	v_mfma_scale_f32_16x16x128_f8f6f4 v[196:199], v[172:179], v[204:211], 0, v143, v143 op_sel:[0,1,0] op_sel_hi:[0,0,0]
	s_setprio 0
	s_barrier
	s_mov_b32 m0, s10
	s_nop 3
	ds_read_b128 v[66:69], v142 offset:16384
	ds_read_b128 v[70:73], v142 offset:17408
	ds_read_b128 v[74:77], v142 offset:18432
	ds_read_b128 v[78:81], v142 offset:19456
	ds_read_b128 v[82:85], v142 offset:20480
	ds_read_b128 v[86:89], v142 offset:21504
	ds_read_b128 v[90:93], v142 offset:22528
	ds_read_b128 v[94:97], v142 offset:23552
	buffer_load_dwordx4 v135, s[80:83], s41 offen lds
	s_add_i32 s42, s41, 0x20000
	s_mov_b32 m0, s11
	s_nop 0
	buffer_load_dwordx4 v135, s[80:83], s42 offen lds
	s_add_i32 s42, s41, 0x40000
	s_mov_b32 m0, s13
	s_nop 0
	buffer_load_dwordx4 v135, s[80:83], s42 offen lds
	s_add_i32 s42, s41, 0x60000
	s_mov_b32 m0, s16
	s_nop 0
	buffer_load_dwordx4 v135, s[80:83], s42 offen lds
	s_mov_b32 m0, s9
	s_add_i32 s42, s39, 0x20000
	buffer_load_dwordx4 v1, s[80:83], s39 offen lds
	s_mov_b32 m0, s17
	s_nop 0
	buffer_load_dwordx4 v1, s[80:83], s42 offen lds
	s_waitcnt vmcnt(8)
	s_waitcnt lgkmcnt(0)
	s_barrier
	s_setprio 1
	s_waitcnt lgkmcnt(6)
	v_mfma_scale_f32_16x16x128_f8f6f4 v[62:65], v[148:155], v[66:73], 0, v143, v143 op_sel:[0,1,0] op_sel_hi:[0,0,0]
	v_mfma_scale_f32_16x16x128_f8f6f4 v[58:61], v[156:163], v[66:73], 0, v143, v143 op_sel:[0,1,0] op_sel_hi:[0,0,0]
	s_waitcnt lgkmcnt(4)
	v_mfma_scale_f32_16x16x128_f8f6f4 v[54:57], v[148:155], v[74:81], 0, v143, v143 op_sel:[0,1,0] op_sel_hi:[0,0,0]
	v_mfma_scale_f32_16x16x128_f8f6f4 v[200:203], v[156:163], v[74:81], 0, v143, v143 op_sel:[0,1,0] op_sel_hi:[0,0,0]
	s_waitcnt lgkmcnt(2)
	v_mfma_scale_f32_16x16x128_f8f6f4 v[204:207], v[148:155], v[82:89], 0, v143, v143 op_sel:[0,1,0] op_sel_hi:[0,0,0]
	v_mfma_scale_f32_16x16x128_f8f6f4 v[208:211], v[156:163], v[82:89], 0, v143, v143 op_sel:[0,1,0] op_sel_hi:[0,0,0]
	s_waitcnt lgkmcnt(0)
	v_mfma_scale_f32_16x16x128_f8f6f4 v[220:223], v[148:155], v[90:97], 0, v143, v143 op_sel:[0,1,0] op_sel_hi:[0,0,0]
	v_mfma_scale_f32_16x16x128_f8f6f4 v[224:227], v[156:163], v[90:97], 0, v143, v143 op_sel:[0,1,0] op_sel_hi:[0,0,0]
	s_setprio 0
	s_setprio 1
	v_mfma_scale_f32_16x16x128_f8f6f4 v[50:53], v[164:171], v[66:73], 0, v143, v143 op_sel:[0,1,0] op_sel_hi:[0,0,0]
	v_mfma_scale_f32_16x16x128_f8f6f4 v[228:231], v[172:179], v[66:73], 0, v143, v143 op_sel:[0,1,0] op_sel_hi:[0,0,0]
	v_mfma_scale_f32_16x16x128_f8f6f4 v[232:235], v[164:171], v[74:81], 0, v143, v143 op_sel:[0,1,0] op_sel_hi:[0,0,0]
	v_mfma_scale_f32_16x16x128_f8f6f4 v[236:239], v[172:179], v[74:81], 0, v143, v143 op_sel:[0,1,0] op_sel_hi:[0,0,0]
	v_mfma_scale_f32_16x16x128_f8f6f4 v[240:243], v[164:171], v[82:89], 0, v143, v143 op_sel:[0,1,0] op_sel_hi:[0,0,0]
	v_mfma_scale_f32_16x16x128_f8f6f4 v[244:247], v[172:179], v[82:89], 0, v143, v143 op_sel:[0,1,0] op_sel_hi:[0,0,0]
	v_mfma_scale_f32_16x16x128_f8f6f4 v[248:251], v[164:171], v[90:97], 0, v143, v143 op_sel:[0,1,0] op_sel_hi:[0,0,0]
	v_mfma_scale_f32_16x16x128_f8f6f4 v[130:133], v[172:179], v[90:97], 0, v143, v143 op_sel:[0,1,0] op_sel_hi:[0,0,0]
	s_setprio 0
	s_barrier
; #define PG8_STAGE(bufoff, goff, voff) do { _Pragma("unroll") for (int _i = 0; _i < 2; ++_i) \
;         __builtin_amdgcn_raw_ptr_buffer_load_lds(rsrc, (PG8_LAS void*)(lds + (bufoff) + ldsw + _i * 8192), 16, (int)(voff), (int)((goff) + _i * p1##voff), 0, 0); } while (0)
; #define PG8_LDA(dst, b, h) do { _Pragma("unroll") for (int m = 0; m < 4; ++m) dst[m] = PG8_LD8(lds + PG8_SA(b, h) + aoff + m * 2048); } while (0)
; #define PG8_LDB(dst, b, h) do { _Pragma("unroll") for (int n = 0; n < 2; ++n) dst[n] = PG8_LD8(lds + PG8_SB(b, h) + boff + n * 2048); } while (0)
; #define PG8_WAIT_V(n) asm volatile("s_waitcnt vmcnt(" #n ")" ::: "memory")
; #define PG8_WAIT_L(n) asm volatile("s_waitcnt lgkmcnt(" #n ")" ::: "memory")
; #define PG8_BAR __builtin_amdgcn_s_barrier()
; #define PG8_SCHED __builtin_amdgcn_sched_barrier(0)
; template <class Epi, class Sched, bool ALIGN_EPI, bool F8 = false, int F8SC = F8_SCALES>
; __device__ __forceinline__ void gemm_phase(PG8_LAS unsigned char* lds, const __amdgpu_buffer_rsrc_t rsrc, const int lda, const int ldb, const int K, const Sched& S, const Epi& E) {
;     ...
;             PG8_LDB(B0, 1, 0); PG8_LDB(B1, 1, 1); PG8_SCHED; PG8_LDA(At, 1, 0); PG8_STAGE(PG8_SA(0, 1), a2 + hsA, voffA);
;             PG8_WAIT_V(8); PG8_WAIT_L(0); PG8_BAR; PG8_MMA(0, 0, At, B0); PG8_MMA(0, 1, At, B1); PG8_BAR; PG8_SCHED;
;             PG8_LDA(At, 1, 1); PG8_STAGE(PG8_SB(1, 0), b3, voffB); PG8_STAGE(PG8_SB(1, 1), b3 + hsB, voffB); PG8_STAGE(PG8_SA(1, 0), a3, voffA);
;             PG8_WAIT_V(8); PG8_WAIT_L(0); PG8_BAR; PG8_MMA(1, 0, At, B0); PG8_MMA(1, 1, At, B1); PG8_BAR; PG8_SCHED;
;         }
	s_nop 4
	ds_read_b128 v[2:5], v144
	ds_read_b128 v[6:9], v144 offset:1024
	ds_read_b128 v[10:13], v144 offset:2048
	ds_read_b128 v[14:17], v144 offset:3072
	ds_read_b128 v[148:151], v145
	ds_read_b128 v[152:155], v145 offset:1024
	ds_read_b128 v[156:159], v145 offset:2048
	ds_read_b128 v[160:163], v145 offset:3072
	s_mov_b32 m0, s18
	s_add_i32 s42, s39, 0x40000
	ds_read_b128 v[18:21], v142 offset:32768
	ds_read_b128 v[22:25], v142 offset:33792
	ds_read_b128 v[26:29], v142 offset:34816
	ds_read_b128 v[30:33], v142 offset:35840
	ds_read_b128 v[34:37], v142 offset:36864
	ds_read_b128 v[38:41], v142 offset:37888
	ds_read_b128 v[42:45], v142 offset:38912
	ds_read_b128 v[46:49], v142 offset:39936
	buffer_load_dwordx4 v1, s[80:83], s42 offen lds
	s_add_i32 s42, s39, 0x60000
	s_mov_b32 m0, s19
	s_nop 0
	buffer_load_dwordx4 v1, s[80:83], s42 offen lds
	s_waitcnt vmcnt(8)
	s_waitcnt lgkmcnt(0)
	s_barrier
	s_setprio 1
	s_waitcnt lgkmcnt(6)
	v_mfma_scale_f32_16x16x128_f8f6f4 v[126:129], v[2:9], v[18:25], v[126:129], v143, v143 op_sel:[0,1,0] op_sel_hi:[0,0,0]
	v_mfma_scale_f32_16x16x128_f8f6f4 v[122:125], v[10:17], v[18:25], v[122:125], v143, v143 op_sel:[0,1,0] op_sel_hi:[0,0,0]
	s_waitcnt lgkmcnt(4)
	v_mfma_scale_f32_16x16x128_f8f6f4 v[118:121], v[2:9], v[26:33], v[118:121], v143, v143 op_sel:[0,1,0] op_sel_hi:[0,0,0]
	v_mfma_scale_f32_16x16x128_f8f6f4 v[110:113], v[10:17], v[26:33], v[110:113], v143, v143 op_sel:[0,1,0] op_sel_hi:[0,0,0]
	s_waitcnt lgkmcnt(2)
	v_mfma_scale_f32_16x16x128_f8f6f4 v[102:105], v[2:9], v[34:41], v[102:105], v143, v143 op_sel:[0,1,0] op_sel_hi:[0,0,0]
	v_mfma_scale_f32_16x16x128_f8f6f4 v[94:97], v[10:17], v[34:41], v[136:139], v143, v143 op_sel:[0,1,0] op_sel_hi:[0,0,0]
	s_waitcnt lgkmcnt(0)
	v_mfma_scale_f32_16x16x128_f8f6f4 v[86:89], v[2:9], v[42:49], v[212:215], v143, v143 op_sel:[0,1,0] op_sel_hi:[0,0,0]
	v_mfma_scale_f32_16x16x128_f8f6f4 v[78:81], v[10:17], v[42:49], v[216:219], v143, v143 op_sel:[0,1,0] op_sel_hi:[0,0,0]
	s_setprio 0
	s_setprio 1
	v_mfma_scale_f32_16x16x128_f8f6f4 v[114:117], v[148:155], v[18:25], v[114:117], v143, v143 op_sel:[0,1,0] op_sel_hi:[0,0,0]
	v_mfma_scale_f32_16x16x128_f8f6f4 v[106:109], v[156:163], v[18:25], v[106:109], v143, v143 op_sel:[0,1,0] op_sel_hi:[0,0,0]
	v_mfma_scale_f32_16x16x128_f8f6f4 v[98:101], v[148:155], v[26:33], v[98:101], v143, v143 op_sel:[0,1,0] op_sel_hi:[0,0,0]
	v_mfma_scale_f32_16x16x128_f8f6f4 v[90:93], v[156:163], v[26:33], v[180:183], v143, v143 op_sel:[0,1,0] op_sel_hi:[0,0,0]
	v_mfma_scale_f32_16x16x128_f8f6f4 v[82:85], v[148:155], v[34:41], v[184:187], v143, v143 op_sel:[0,1,0] op_sel_hi:[0,0,0]
	v_mfma_scale_f32_16x16x128_f8f6f4 v[74:77], v[156:163], v[34:41], v[188:191], v143, v143 op_sel:[0,1,0] op_sel_hi:[0,0,0]
	v_mfma_scale_f32_16x16x128_f8f6f4 v[70:73], v[148:155], v[42:49], v[192:195], v143, v143 op_sel:[0,1,0] op_sel_hi:[0,0,0]
	v_mfma_scale_f32_16x16x128_f8f6f4 v[66:69], v[156:163], v[42:49], v[196:199], v143, v143 op_sel:[0,1,0] op_sel_hi:[0,0,0]
	s_setprio 0
	s_barrier
	s_mov_b32 m0, s21
	s_add_i32 s42, s41, 0x80
	ds_read_b128 v[164:167], v142 offset:49152
	ds_read_b128 v[168:171], v142 offset:50176
	ds_read_b128 v[172:175], v142 offset:51200
	ds_read_b128 v[176:179], v142 offset:52224
	ds_read_b128 v[180:183], v142 offset:53248
	ds_read_b128 v[184:187], v142 offset:54272
	ds_read_b128 v[188:191], v142 offset:55296
	ds_read_b128 v[192:195], v142 offset:56320
	buffer_load_dwordx4 v135, s[80:83], s42 offen lds
	s_add_i32 s42, s41, 0x20080
	s_mov_b32 m0, s22
	s_add_i32 s39, s39, 0x20080
	buffer_load_dwordx4 v135, s[80:83], s42 offen lds
	s_add_i32 s42, s41, 0x40080
	s_mov_b32 m0, s25
	s_add_i32 s41, s41, 0x60080
	buffer_load_dwordx4 v135, s[80:83], s42 offen lds
	s_mov_b32 m0, s26
	s_nop 0
	buffer_load_dwordx4 v135, s[80:83], s41 offen lds
	s_mov_b32 m0, s23
	s_nop 0
	buffer_load_dwordx4 v1, s[80:83], s40 offen lds
	s_mov_b32 m0, s24
	s_nop 0
	buffer_load_dwordx4 v1, s[80:83], s39 offen lds
	s_waitcnt vmcnt(8)
	s_waitcnt lgkmcnt(0)
	s_barrier
	s_setprio 1
	s_waitcnt lgkmcnt(6)
	v_mfma_scale_f32_16x16x128_f8f6f4 v[62:65], v[2:9], v[164:171], v[62:65], v143, v143 op_sel:[0,1,0] op_sel_hi:[0,0,0]
	v_mfma_scale_f32_16x16x128_f8f6f4 v[58:61], v[10:17], v[164:171], v[58:61], v143, v143 op_sel:[0,1,0] op_sel_hi:[0,0,0]
	s_waitcnt lgkmcnt(4)
	v_mfma_scale_f32_16x16x128_f8f6f4 v[54:57], v[2:9], v[172:179], v[54:57], v143, v143 op_sel:[0,1,0] op_sel_hi:[0,0,0]
	v_mfma_scale_f32_16x16x128_f8f6f4 v[46:49], v[10:17], v[172:179], v[200:203], v143, v143 op_sel:[0,1,0] op_sel_hi:[0,0,0]
	s_waitcnt lgkmcnt(2)
	v_mfma_scale_f32_16x16x128_f8f6f4 v[38:41], v[2:9], v[180:187], v[204:207], v143, v143 op_sel:[0,1,0] op_sel_hi:[0,0,0]
	v_mfma_scale_f32_16x16x128_f8f6f4 v[30:33], v[10:17], v[180:187], v[208:211], v143, v143 op_sel:[0,1,0] op_sel_hi:[0,0,0]
	s_waitcnt lgkmcnt(0)
	v_mfma_scale_f32_16x16x128_f8f6f4 v[22:25], v[2:9], v[188:195], v[220:223], v143, v143 op_sel:[0,1,0] op_sel_hi:[0,0,0]
	v_mfma_scale_f32_16x16x128_f8f6f4 v[14:17], v[10:17], v[188:195], v[224:227], v143, v143 op_sel:[0,1,0] op_sel_hi:[0,0,0]
	s_setprio 0
	s_setprio 1
	v_mfma_scale_f32_16x16x128_f8f6f4 v[50:53], v[148:155], v[164:171], v[50:53], v143, v143 op_sel:[0,1,0] op_sel_hi:[0,0,0]
	v_mfma_scale_f32_16x16x128_f8f6f4 v[42:45], v[156:163], v[164:171], v[228:231], v143, v143 op_sel:[0,1,0] op_sel_hi:[0,0,0]
	v_mfma_scale_f32_16x16x128_f8f6f4 v[34:37], v[148:155], v[172:179], v[232:235], v143, v143 op_sel:[0,1,0] op_sel_hi:[0,0,0]
	v_mfma_scale_f32_16x16x128_f8f6f4 v[26:29], v[156:163], v[172:179], v[236:239], v143, v143 op_sel:[0,1,0] op_sel_hi:[0,0,0]
	v_mfma_scale_f32_16x16x128_f8f6f4 v[18:21], v[148:155], v[180:187], v[240:243], v143, v143 op_sel:[0,1,0] op_sel_hi:[0,0,0]
	v_mfma_scale_f32_16x16x128_f8f6f4 v[10:13], v[156:163], v[180:187], v[244:247], v143, v143 op_sel:[0,1,0] op_sel_hi:[0,0,0]
	v_mfma_scale_f32_16x16x128_f8f6f4 v[6:9], v[148:155], v[188:195], v[248:251], v143, v143 op_sel:[0,1,0] op_sel_hi:[0,0,0]
	v_mfma_scale_f32_16x16x128_f8f6f4 v[2:5], v[156:163], v[188:195], v[130:133], v143, v143 op_sel:[0,1,0] op_sel_hi:[0,0,0]
	s_setprio 0
	s_barrier
	s_add_i32 s38, s38, 2
	s_addk_i32 s36, 0x100
	s_addk_i32 s37, 0x100
	s_cmp_gt_u32 s38, 13
	s_cbranch_scc0 .LBB0_739
	s_branch .Lpeel_after_739

; #define PG8_BAR __builtin_amdgcn_s_barrier()
; template <class Epi, class Sched, bool ALIGN_EPI, bool F8 = false, int F8SC = F8_SCALES>
; __device__ __forceinline__ void gemm_phase(PG8_LAS unsigned char* lds, const __amdgpu_buffer_rsrc_t rsrc, const int lda, const int ldb, const int K, const Sched& S, const Epi& E) {
;     ...
;         if constexpr (ALIGN_EPI) { if (wr == 0) PG8_BAR; }
.Lpeel_after_739:
	s_and_b64 vcc, exec, s[6:7]
	s_cbranch_vccz .LBB0_742
	s_barrier

;     __device__ __forceinline__ bool next(int i, Unit& u) const { u.aux = 0; return t.map(i, u.pm, u.pn); }
;     __device__ __forceinline__ bool next(int i, Unit& u) const { u.aux = i & 1; return t.map(i >> 1, u.pm, u.pn); }
; #define PG8_WAIT_V(n) asm volatile("s_waitcnt vmcnt(" #n ")" ::: "memory")
; #define PG8_BAR __builtin_amdgcn_s_barrier()
; template <class Epi, class Sched, bool ALIGN_EPI, bool F8 = false, int F8SC = F8_SCALES>
; __device__ __forceinline__ void gemm_phase(PG8_LAS unsigned char* lds, const __amdgpu_buffer_rsrc_t rsrc, const int lda, const int ldb, const int K, const Sched& S, const Epi& E) {
;     ...
;     Unit cur, nxt; int ui = 0;
;     if (!S.next(0, cur)) return;
;     f32x4 acc[2][2][4][2];
;     PG8_ZERO();
;     i32x8 At[4], B0[2], B1[2];
;     unsigned cA, cB; S.bases(cur, cA, cB); cA = __builtin_amdgcn_readfirstlane(cA); cB = __builtin_amdgcn_readfirstlane(cB);
;     PG8_STAGE(PG8_SB(0, 0), cB, voffB); PG8_STAGE(PG8_SB(0, 1), cB + hsB, voffB); PG8_STAGE(PG8_SA(0, 0), cA, voffA); PG8_STAGE(PG8_SA(0, 1), cA + hsA, voffA);
;     if (wr == 1) PG8_BAR;
;     PG8_WAIT_V(2); PG8_BAR;
;     PG8_STAGE(PG8_SB(1, 0), cB + kstep, voffB); PG8_STAGE(PG8_SA(1, 0), cA + kstep, voffA); PG8_STAGE(PG8_SB(1, 1), cB + hsB + kstep, voffB);
;     PG8_WAIT_V(6); PG8_BAR;
;     for (;;) {
;         const bool has_next = S.next(ui + 1, nxt);
;         unsigned nA = cA, nB = cB; if (has_next) { S.bases(nxt, nA, nB); nA = __builtin_amdgcn_readfirstlane(nA); nB = __builtin_amdgcn_readfirstlane(nB); }
; #pragma unroll 1
;         for (int t = 0; t < nt; t += 2) {
;             const bool last = (t == nt - 2);
;             const unsigned a1 = cA + (unsigned)(t + 1) * kstep;
;             const unsigned a2 = last ? nA : cA + (unsigned)(t + 2) * kstep, b2 = last ? nB : cB + (unsigned)(t + 2) * kstep;
;             const unsigned a3 = a2 + kstep, b3 = b2 + kstep;
;             PG8_LDB(B0, 0, 0); PG8_LDB(B1, 0, 1); PG8_SCHED; PG8_LDA(At, 0, 0); PG8_STAGE(PG8_SA(1, 1), a1 + hsA, voffA);
;             PG8_WAIT_V(8); PG8_WAIT_L(0); PG8_BAR; PG8_MMA(0, 0, At, B0); PG8_MMA(0, 1, At, B1); PG8_BAR; PG8_SCHED;
;             PG8_LDA(At, 0, 1); PG8_STAGE(PG8_SB(0, 0), b2, voffB); PG8_STAGE(PG8_SB(0, 1), b2 + hsB, voffB); PG8_STAGE(PG8_SA(0, 0), a2, voffA);
;             PG8_WAIT_V(8); PG8_WAIT_L(0); PG8_BAR; PG8_MMA(1, 0, At, B0); PG8_MMA(1, 1, At, B1); PG8_BAR; PG8_SCHED;
.LBB0_764:
	s_add_i32 s4, s38, 0x60080
	s_add_i32 s5, s37, 0x100
	s_mov_b32 s37, -2
	ds_read_b128 v[146:149], v139
	ds_read_b128 v[150:153], v139 offset:1024
	ds_read_b128 v[154:157], v139 offset:2048
	ds_read_b128 v[158:161], v139 offset:3072
	ds_read_b128 v[162:165], v140
	ds_read_b128 v[166:169], v140 offset:1024
	ds_read_b128 v[170:173], v140 offset:2048
	ds_read_b128 v[174:177], v140 offset:3072
	s_add_i32 s38, s4, 0xfffa0080
	s_cmp_eq_u32 s37, 12
	s_cselect_b32 s38, s33, s38
	s_cselect_b32 s40, s34, s5
	s_add_i32 s39, s38, 0x80
	s_add_i32 s41, s4, 0xfffe0000
	s_mov_b32 s80, s96
	s_mov_b32 m0, s27
	ds_read_b128 v[178:181], v141
	ds_read_b128 v[182:185], v141 offset:1024
	ds_read_b128 v[186:189], v141 offset:2048
	ds_read_b128 v[190:193], v141 offset:3072
	ds_read_b128 v[194:197], v141 offset:4096
	ds_read_b128 v[198:201], v141 offset:5120
	ds_read_b128 v[202:205], v141 offset:6144
	ds_read_b128 v[206:209], v141 offset:7168
	buffer_load_dwordx4 v1, s[80:83], s41 offen lds
	s_mov_b32 m0, s28
	s_nop 0
	buffer_load_dwordx4 v1, s[80:83], s4 offen lds
	s_waitcnt vmcnt(8)
	s_waitcnt lgkmcnt(0)
	s_barrier
	s_setprio 1
	s_waitcnt lgkmcnt(6)
	v_mfma_scale_f32_16x16x128_f8f6f4 v[126:129], v[146:153], v[178:185], 0, v142, v142 op_sel:[0,1,0] op_sel_hi:[0,0,0]
	v_mfma_scale_f32_16x16x128_f8f6f4 v[118:121], v[154:161], v[178:185], 0, v142, v142 op_sel:[0,1,0] op_sel_hi:[0,0,0]
	s_waitcnt lgkmcnt(4)
	v_mfma_scale_f32_16x16x128_f8f6f4 v[110:113], v[146:153], v[186:193], 0, v142, v142 op_sel:[0,1,0] op_sel_hi:[0,0,0]
	v_mfma_scale_f32_16x16x128_f8f6f4 v[102:105], v[154:161], v[186:193], 0, v142, v142 op_sel:[0,1,0] op_sel_hi:[0,0,0]
	s_waitcnt lgkmcnt(2)
	v_mfma_scale_f32_16x16x128_f8f6f4 v[210:213], v[146:153], v[194:201], 0, v142, v142 op_sel:[0,1,0] op_sel_hi:[0,0,0]
	v_mfma_scale_f32_16x16x128_f8f6f4 v[214:217], v[154:161], v[194:201], 0, v142, v142 op_sel:[0,1,0] op_sel_hi:[0,0,0]
	s_waitcnt lgkmcnt(0)
	v_mfma_scale_f32_16x16x128_f8f6f4 v[218:221], v[146:153], v[202:209], 0, v142, v142 op_sel:[0,1,0] op_sel_hi:[0,0,0]
	v_mfma_scale_f32_16x16x128_f8f6f4 v[222:225], v[154:161], v[202:209], 0, v142, v142 op_sel:[0,1,0] op_sel_hi:[0,0,0]
	s_setprio 0
	s_setprio 1
	v_mfma_scale_f32_16x16x128_f8f6f4 v[122:125], v[162:169], v[178:185], 0, v142, v142 op_sel:[0,1,0] op_sel_hi:[0,0,0]
	v_mfma_scale_f32_16x16x128_f8f6f4 v[114:117], v[170:177], v[178:185], 0, v142, v142 op_sel:[0,1,0] op_sel_hi:[0,0,0]
	v_mfma_scale_f32_16x16x128_f8f6f4 v[106:109], v[162:169], v[186:193], 0, v142, v142 op_sel:[0,1,0] op_sel_hi:[0,0,0]
	v_mfma_scale_f32_16x16x128_f8f6f4 v[98:101], v[170:177], v[186:193], 0, v142, v142 op_sel:[0,1,0] op_sel_hi:[0,0,0]
	v_mfma_scale_f32_16x16x128_f8f6f4 v[178:181], v[162:169], v[194:201], 0, v142, v142 op_sel:[0,1,0] op_sel_hi:[0,0,0]
	v_mfma_scale_f32_16x16x128_f8f6f4 v[182:185], v[170:177], v[194:201], 0, v142, v142 op_sel:[0,1,0] op_sel_hi:[0,0,0]
	v_mfma_scale_f32_16x16x128_f8f6f4 v[186:189], v[162:169], v[202:209], 0, v142, v142 op_sel:[0,1,0] op_sel_hi:[0,0,0]
	v_mfma_scale_f32_16x16x128_f8f6f4 v[190:193], v[170:177], v[202:209], 0, v142, v142 op_sel:[0,1,0] op_sel_hi:[0,0,0]
	s_setprio 0
	s_barrier
	s_mov_b32 m0, s10
	s_nop 3
	ds_read_b128 v[66:69], v141 offset:16384
	ds_read_b128 v[70:73], v141 offset:17408
	ds_read_b128 v[74:77], v141 offset:18432
	ds_read_b128 v[78:81], v141 offset:19456
	ds_read_b128 v[82:85], v141 offset:20480
	ds_read_b128 v[86:89], v141 offset:21504
	ds_read_b128 v[90:93], v141 offset:22528
	ds_read_b128 v[94:97], v141 offset:23552
	buffer_load_dwordx4 v138, s[80:83], s40 offen lds
	s_add_i32 s41, s40, 0x20000
	s_mov_b32 m0, s11
	s_nop 0
	buffer_load_dwordx4 v138, s[80:83], s41 offen lds
	s_add_i32 s41, s40, 0x40000
	s_mov_b32 m0, s13
	s_nop 0
	buffer_load_dwordx4 v138, s[80:83], s41 offen lds
	s_add_i32 s41, s40, 0x60000
	s_mov_b32 m0, s16
	s_nop 0
	buffer_load_dwordx4 v138, s[80:83], s41 offen lds
	s_mov_b32 m0, s9
	s_add_i32 s41, s38, 0x20000
	buffer_load_dwordx4 v1, s[80:83], s38 offen lds
	s_mov_b32 m0, s17
	s_nop 0
	buffer_load_dwordx4 v1, s[80:83], s41 offen lds
	s_waitcnt vmcnt(8)
	s_waitcnt lgkmcnt(0)
	s_barrier
	s_setprio 1
	s_waitcnt lgkmcnt(6)
	v_mfma_scale_f32_16x16x128_f8f6f4 v[62:65], v[146:153], v[66:73], 0, v142, v142 op_sel:[0,1,0] op_sel_hi:[0,0,0]
	v_mfma_scale_f32_16x16x128_f8f6f4 v[54:57], v[154:161], v[66:73], 0, v142, v142 op_sel:[0,1,0] op_sel_hi:[0,0,0]
	s_waitcnt lgkmcnt(4)
	v_mfma_scale_f32_16x16x128_f8f6f4 v[46:49], v[146:153], v[74:81], 0, v142, v142 op_sel:[0,1,0] op_sel_hi:[0,0,0]
	v_mfma_scale_f32_16x16x128_f8f6f4 v[202:205], v[154:161], v[74:81], 0, v142, v142 op_sel:[0,1,0] op_sel_hi:[0,0,0]
	s_waitcnt lgkmcnt(2)
	v_mfma_scale_f32_16x16x128_f8f6f4 v[206:209], v[146:153], v[82:89], 0, v142, v142 op_sel:[0,1,0] op_sel_hi:[0,0,0]
	v_mfma_scale_f32_16x16x128_f8f6f4 v[226:229], v[154:161], v[82:89], 0, v142, v142 op_sel:[0,1,0] op_sel_hi:[0,0,0]
	s_waitcnt lgkmcnt(0)
	v_mfma_scale_f32_16x16x128_f8f6f4 v[230:233], v[146:153], v[90:97], 0, v142, v142 op_sel:[0,1,0] op_sel_hi:[0,0,0]
	v_mfma_scale_f32_16x16x128_f8f6f4 v[234:237], v[154:161], v[90:97], 0, v142, v142 op_sel:[0,1,0] op_sel_hi:[0,0,0]
	s_setprio 0
	s_setprio 1
	v_mfma_scale_f32_16x16x128_f8f6f4 v[58:61], v[162:169], v[66:73], 0, v142, v142 op_sel:[0,1,0] op_sel_hi:[0,0,0]
	v_mfma_scale_f32_16x16x128_f8f6f4 v[50:53], v[170:177], v[66:73], 0, v142, v142 op_sel:[0,1,0] op_sel_hi:[0,0,0]
	v_mfma_scale_f32_16x16x128_f8f6f4 v[42:45], v[162:169], v[74:81], 0, v142, v142 op_sel:[0,1,0] op_sel_hi:[0,0,0]
	v_mfma_scale_f32_16x16x128_f8f6f4 v[238:241], v[170:177], v[74:81], 0, v142, v142 op_sel:[0,1,0] op_sel_hi:[0,0,0]
	v_mfma_scale_f32_16x16x128_f8f6f4 v[242:245], v[162:169], v[82:89], 0, v142, v142 op_sel:[0,1,0] op_sel_hi:[0,0,0]
	v_mfma_scale_f32_16x16x128_f8f6f4 v[246:249], v[170:177], v[82:89], 0, v142, v142 op_sel:[0,1,0] op_sel_hi:[0,0,0]
	v_mfma_scale_f32_16x16x128_f8f6f4 v[250:253], v[162:169], v[90:97], 0, v142, v142 op_sel:[0,1,0] op_sel_hi:[0,0,0]
	v_mfma_scale_f32_16x16x128_f8f6f4 v[130:133], v[170:177], v[90:97], 0, v142, v142 op_sel:[0,1,0] op_sel_hi:[0,0,0]
	s_setprio 0
	s_barrier
; #define PG8_STAGE(bufoff, goff, voff) do { _Pragma("unroll") for (int _i = 0; _i < 2; ++_i) \
;         __builtin_amdgcn_raw_ptr_buffer_load_lds(rsrc, (PG8_LAS void*)(lds + (bufoff) + ldsw + _i * 8192), 16, (int)(voff), (int)((goff) + _i * p1##voff), 0, 0); } while (0)
; #define PG8_LDA(dst, b, h) do { _Pragma("unroll") for (int m = 0; m < 4; ++m) dst[m] = PG8_LD8(lds + PG8_SA(b, h) + aoff + m * 2048); } while (0)
; #define PG8_LDB(dst, b, h) do { _Pragma("unroll") for (int n = 0; n < 2; ++n) dst[n] = PG8_LD8(lds + PG8_SB(b, h) + boff + n * 2048); } while (0)
; #define PG8_WAIT_V(n) asm volatile("s_waitcnt vmcnt(" #n ")" ::: "memory")
; #define PG8_WAIT_L(n) asm volatile("s_waitcnt lgkmcnt(" #n ")" ::: "memory")
; #define PG8_BAR __builtin_amdgcn_s_barrier()
; #define PG8_SCHED __builtin_amdgcn_sched_barrier(0)
; template <class Epi, class Sched, bool ALIGN_EPI, bool F8 = false, int F8SC = F8_SCALES>
; __device__ __forceinline__ void gemm_phase(PG8_LAS unsigned char* lds, const __amdgpu_buffer_rsrc_t rsrc, const int lda, const int ldb, const int K, const Sched& S, const Epi& E) {
;     ...
;             PG8_LDB(B0, 1, 0); PG8_LDB(B1, 1, 1); PG8_SCHED; PG8_LDA(At, 1, 0); PG8_STAGE(PG8_SA(0, 1), a2 + hsA, voffA);
;             PG8_WAIT_V(8); PG8_WAIT_L(0); PG8_BAR; PG8_MMA(0, 0, At, B0); PG8_MMA(0, 1, At, B1); PG8_BAR; PG8_SCHED;
;             PG8_LDA(At, 1, 1); PG8_STAGE(PG8_SB(1, 0), b3, voffB); PG8_STAGE(PG8_SB(1, 1), b3 + hsB, voffB); PG8_STAGE(PG8_SA(1, 0), a3, voffA);
;             PG8_WAIT_V(8); PG8_WAIT_L(0); PG8_BAR; PG8_MMA(1, 0, At, B0); PG8_MMA(1, 1, At, B1); PG8_BAR; PG8_SCHED;
;         }
	s_nop 4
	ds_read_b128 v[2:5], v143
	ds_read_b128 v[6:9], v143 offset:1024
	ds_read_b128 v[146:149], v143 offset:2048
	ds_read_b128 v[150:153], v143 offset:3072
	ds_read_b128 v[154:157], v144
	ds_read_b128 v[158:161], v144 offset:1024
	ds_read_b128 v[162:165], v144 offset:2048
	ds_read_b128 v[166:169], v144 offset:3072
	s_mov_b32 m0, s18
	s_add_i32 s41, s38, 0x40000
	ds_read_b128 v[10:13], v141 offset:32768
	ds_read_b128 v[14:17], v141 offset:33792
	ds_read_b128 v[18:21], v141 offset:34816
	ds_read_b128 v[22:25], v141 offset:35840
	ds_read_b128 v[26:29], v141 offset:36864
	ds_read_b128 v[30:33], v141 offset:37888
	ds_read_b128 v[34:37], v141 offset:38912
	ds_read_b128 v[38:41], v141 offset:39936
	buffer_load_dwordx4 v1, s[80:83], s41 offen lds
	s_add_i32 s41, s38, 0x60000
	s_mov_b32 m0, s19
	s_nop 0
	buffer_load_dwordx4 v1, s[80:83], s41 offen lds
	s_waitcnt vmcnt(8)
	s_waitcnt lgkmcnt(0)
	s_barrier
	s_setprio 1
	s_waitcnt lgkmcnt(6)
	v_mfma_scale_f32_16x16x128_f8f6f4 v[126:129], v[2:9], v[10:17], v[126:129], v142, v142 op_sel:[0,1,0] op_sel_hi:[0,0,0]
	v_mfma_scale_f32_16x16x128_f8f6f4 v[118:121], v[146:153], v[10:17], v[118:121], v142, v142 op_sel:[0,1,0] op_sel_hi:[0,0,0]
	s_waitcnt lgkmcnt(4)
	v_mfma_scale_f32_16x16x128_f8f6f4 v[110:113], v[2:9], v[18:25], v[110:113], v142, v142 op_sel:[0,1,0] op_sel_hi:[0,0,0]
	v_mfma_scale_f32_16x16x128_f8f6f4 v[102:105], v[146:153], v[18:25], v[102:105], v142, v142 op_sel:[0,1,0] op_sel_hi:[0,0,0]
	s_waitcnt lgkmcnt(2)
	v_mfma_scale_f32_16x16x128_f8f6f4 v[94:97], v[2:9], v[26:33], v[210:213], v142, v142 op_sel:[0,1,0] op_sel_hi:[0,0,0]
	v_mfma_scale_f32_16x16x128_f8f6f4 v[86:89], v[146:153], v[26:33], v[214:217], v142, v142 op_sel:[0,1,0] op_sel_hi:[0,0,0]
	s_waitcnt lgkmcnt(0)
	v_mfma_scale_f32_16x16x128_f8f6f4 v[78:81], v[2:9], v[34:41], v[218:221], v142, v142 op_sel:[0,1,0] op_sel_hi:[0,0,0]
	v_mfma_scale_f32_16x16x128_f8f6f4 v[70:73], v[146:153], v[34:41], v[222:225], v142, v142 op_sel:[0,1,0] op_sel_hi:[0,0,0]
	s_setprio 0
	s_setprio 1
	v_mfma_scale_f32_16x16x128_f8f6f4 v[122:125], v[154:161], v[10:17], v[122:125], v142, v142 op_sel:[0,1,0] op_sel_hi:[0,0,0]
	v_mfma_scale_f32_16x16x128_f8f6f4 v[114:117], v[162:169], v[10:17], v[114:117], v142, v142 op_sel:[0,1,0] op_sel_hi:[0,0,0]
	v_mfma_scale_f32_16x16x128_f8f6f4 v[106:109], v[154:161], v[18:25], v[106:109], v142, v142 op_sel:[0,1,0] op_sel_hi:[0,0,0]
	v_mfma_scale_f32_16x16x128_f8f6f4 v[98:101], v[162:169], v[18:25], v[98:101], v142, v142 op_sel:[0,1,0] op_sel_hi:[0,0,0]
	v_mfma_scale_f32_16x16x128_f8f6f4 v[90:93], v[154:161], v[26:33], v[178:181], v142, v142 op_sel:[0,1,0] op_sel_hi:[0,0,0]
	v_mfma_scale_f32_16x16x128_f8f6f4 v[82:85], v[162:169], v[26:33], v[182:185], v142, v142 op_sel:[0,1,0] op_sel_hi:[0,0,0]
	v_mfma_scale_f32_16x16x128_f8f6f4 v[74:77], v[154:161], v[34:41], v[186:189], v142, v142 op_sel:[0,1,0] op_sel_hi:[0,0,0]
	v_mfma_scale_f32_16x16x128_f8f6f4 v[66:69], v[162:169], v[34:41], v[190:193], v142, v142 op_sel:[0,1,0] op_sel_hi:[0,0,0]
	s_setprio 0
	s_barrier
	s_mov_b32 m0, s21
	s_add_i32 s41, s40, 0x80
	ds_read_b128 v[170:173], v141 offset:49152
	ds_read_b128 v[174:177], v141 offset:50176
	ds_read_b128 v[178:181], v141 offset:51200
	ds_read_b128 v[182:185], v141 offset:52224
	ds_read_b128 v[186:189], v141 offset:53248
	ds_read_b128 v[190:193], v141 offset:54272
	ds_read_b128 v[194:197], v141 offset:55296
	ds_read_b128 v[198:201], v141 offset:56320
	buffer_load_dwordx4 v138, s[80:83], s41 offen lds
	s_add_i32 s41, s40, 0x20080
	s_mov_b32 m0, s22
	s_add_i32 s38, s38, 0x20080
	buffer_load_dwordx4 v138, s[80:83], s41 offen lds
	s_add_i32 s41, s40, 0x40080
	s_mov_b32 m0, s25
	s_add_i32 s40, s40, 0x60080
	buffer_load_dwordx4 v138, s[80:83], s41 offen lds
	s_mov_b32 m0, s26
	s_nop 0
	buffer_load_dwordx4 v138, s[80:83], s40 offen lds
	s_mov_b32 m0, s23
	s_nop 0
	buffer_load_dwordx4 v1, s[80:83], s39 offen lds
	s_mov_b32 m0, s24
	s_nop 0
	buffer_load_dwordx4 v1, s[80:83], s38 offen lds
	s_waitcnt vmcnt(8)
	s_waitcnt lgkmcnt(0)
	s_barrier
	s_setprio 1
	s_waitcnt lgkmcnt(6)
	v_mfma_scale_f32_16x16x128_f8f6f4 v[62:65], v[2:9], v[170:177], v[62:65], v142, v142 op_sel:[0,1,0] op_sel_hi:[0,0,0]
	v_mfma_scale_f32_16x16x128_f8f6f4 v[54:57], v[146:153], v[170:177], v[54:57], v142, v142 op_sel:[0,1,0] op_sel_hi:[0,0,0]
	s_waitcnt lgkmcnt(4)
	v_mfma_scale_f32_16x16x128_f8f6f4 v[46:49], v[2:9], v[178:185], v[46:49], v142, v142 op_sel:[0,1,0] op_sel_hi:[0,0,0]
	v_mfma_scale_f32_16x16x128_f8f6f4 v[38:41], v[146:153], v[178:185], v[202:205], v142, v142 op_sel:[0,1,0] op_sel_hi:[0,0,0]
	s_waitcnt lgkmcnt(2)
	v_mfma_scale_f32_16x16x128_f8f6f4 v[30:33], v[2:9], v[186:193], v[206:209], v142, v142 op_sel:[0,1,0] op_sel_hi:[0,0,0]
	v_mfma_scale_f32_16x16x128_f8f6f4 v[22:25], v[146:153], v[186:193], v[226:229], v142, v142 op_sel:[0,1,0] op_sel_hi:[0,0,0]
	s_waitcnt lgkmcnt(0)
	v_mfma_scale_f32_16x16x128_f8f6f4 v[14:17], v[2:9], v[194:201], v[230:233], v142, v142 op_sel:[0,1,0] op_sel_hi:[0,0,0]
	v_mfma_scale_f32_16x16x128_f8f6f4 v[6:9], v[146:153], v[194:201], v[234:237], v142, v142 op_sel:[0,1,0] op_sel_hi:[0,0,0]
	s_setprio 0
	s_setprio 1
	v_mfma_scale_f32_16x16x128_f8f6f4 v[58:61], v[154:161], v[170:177], v[58:61], v142, v142 op_sel:[0,1,0] op_sel_hi:[0,0,0]
	v_mfma_scale_f32_16x16x128_f8f6f4 v[50:53], v[162:169], v[170:177], v[50:53], v142, v142 op_sel:[0,1,0] op_sel_hi:[0,0,0]
	v_mfma_scale_f32_16x16x128_f8f6f4 v[42:45], v[154:161], v[178:185], v[42:45], v142, v142 op_sel:[0,1,0] op_sel_hi:[0,0,0]
	v_mfma_scale_f32_16x16x128_f8f6f4 v[34:37], v[162:169], v[178:185], v[238:241], v142, v142 op_sel:[0,1,0] op_sel_hi:[0,0,0]
	v_mfma_scale_f32_16x16x128_f8f6f4 v[26:29], v[154:161], v[186:193], v[242:245], v142, v142 op_sel:[0,1,0] op_sel_hi:[0,0,0]
	v_mfma_scale_f32_16x16x128_f8f6f4 v[18:21], v[162:169], v[186:193], v[246:249], v142, v142 op_sel:[0,1,0] op_sel_hi:[0,0,0]
	v_mfma_scale_f32_16x16x128_f8f6f4 v[10:13], v[154:161], v[194:201], v[250:253], v142, v142 op_sel:[0,1,0] op_sel_hi:[0,0,0]
	v_mfma_scale_f32_16x16x128_f8f6f4 v[2:5], v[162:169], v[194:201], v[130:133], v142, v142 op_sel:[0,1,0] op_sel_hi:[0,0,0]
	s_setprio 0
	s_barrier
	s_add_i32 s37, s37, 2
	s_addk_i32 s4, 0x100
	s_addk_i32 s5, 0x100
	s_cmp_gt_u32 s37, 13
	s_cbranch_scc0 .LBB0_765
	s_branch .Lpeel_after_765

;     __device__ __forceinline__ bool next(int i, Unit& u) const { u.aux = 0; return t.map(i, u.pm, u.pn); }
;     __device__ __forceinline__ bool next(int i, Unit& u) const { u.aux = i & 1; return t.map(i >> 1, u.pm, u.pn); }
; #define PG8_WAIT_V(n) asm volatile("s_waitcnt vmcnt(" #n ")" ::: "memory")
; #define PG8_BAR __builtin_amdgcn_s_barrier()
; template <class Epi, class Sched, bool ALIGN_EPI, bool F8 = false, int F8SC = F8_SCALES>
; __device__ __forceinline__ void gemm_phase(PG8_LAS unsigned char* lds, const __amdgpu_buffer_rsrc_t rsrc, const int lda, const int ldb, const int K, const Sched& S, const Epi& E) {
;     ...
;     Unit cur, nxt; int ui = 0;
;     if (!S.next(0, cur)) return;
;     f32x4 acc[2][2][4][2];
;     PG8_ZERO();
;     i32x8 At[4], B0[2], B1[2];
;     unsigned cA, cB; S.bases(cur, cA, cB); cA = __builtin_amdgcn_readfirstlane(cA); cB = __builtin_amdgcn_readfirstlane(cB);
;     PG8_STAGE(PG8_SB(0, 0), cB, voffB); PG8_STAGE(PG8_SB(0, 1), cB + hsB, voffB); PG8_STAGE(PG8_SA(0, 0), cA, voffA); PG8_STAGE(PG8_SA(0, 1), cA + hsA, voffA);
;     if (wr == 1) PG8_BAR;
;     PG8_WAIT_V(2); PG8_BAR;
;     PG8_STAGE(PG8_SB(1, 0), cB + kstep, voffB); PG8_STAGE(PG8_SA(1, 0), cA + kstep, voffA); PG8_STAGE(PG8_SB(1, 1), cB + hsB + kstep, voffB);
;     PG8_WAIT_V(6); PG8_BAR;
;     for (;;) {
;         const bool has_next = S.next(ui + 1, nxt);
;         unsigned nA = cA, nB = cB; if (has_next) { S.bases(nxt, nA, nB); nA = __builtin_amdgcn_readfirstlane(nA); nB = __builtin_amdgcn_readfirstlane(nB); }
; #pragma unroll 1
;         for (int t = 0; t < nt; t += 2) {
;             const bool last = (t == nt - 2);
;             const unsigned a1 = cA + (unsigned)(t + 1) * kstep;
;             const unsigned a2 = last ? nA : cA + (unsigned)(t + 2) * kstep, b2 = last ? nB : cB + (unsigned)(t + 2) * kstep;
;             const unsigned a3 = a2 + kstep, b3 = b2 + kstep;
;             PG8_LDB(B0, 0, 0); PG8_LDB(B1, 0, 1); PG8_SCHED; PG8_LDA(At, 0, 0); PG8_STAGE(PG8_SA(1, 1), a1 + hsA, voffA);
;             PG8_WAIT_V(8); PG8_WAIT_L(0); PG8_BAR; PG8_MMA(0, 0, At, B0); PG8_MMA(0, 1, At, B1); PG8_BAR; PG8_SCHED;
;             PG8_LDA(At, 0, 1); PG8_STAGE(PG8_SB(0, 0), b2, voffB); PG8_STAGE(PG8_SB(0, 1), b2 + hsB, voffB); PG8_STAGE(PG8_SA(0, 0), a2, voffA);
;             PG8_WAIT_V(8); PG8_WAIT_L(0); PG8_BAR; PG8_MMA(1, 0, At, B0); PG8_MMA(1, 1, At, B1); PG8_BAR; PG8_SCHED;
.LBB0_790:
	s_add_i32 s39, s39, 0x60080
	s_addk_i32 s40, 0x100
	s_mov_b32 s41, -2
	ds_read_b128 v[142:145], v135
	ds_read_b128 v[146:149], v135 offset:1024
	ds_read_b128 v[150:153], v135 offset:2048
	ds_read_b128 v[154:157], v135 offset:3072
	ds_read_b128 v[158:161], v136
	ds_read_b128 v[162:165], v136 offset:1024
	ds_read_b128 v[166:169], v136 offset:2048
	ds_read_b128 v[170:173], v136 offset:3072
	s_add_i32 s42, s39, 0xfffa0080
	s_cmp_eq_u32 s41, 12
	s_cselect_b32 s42, s4, s42
	s_cselect_b32 s44, s5, s40
	s_add_i32 s43, s42, 0x80
	s_add_i32 s45, s39, 0xfffe0000
	s_mov_b32 s80, s96
	s_mov_b32 m0, s31
	ds_read_b128 v[174:177], v137
	ds_read_b128 v[178:181], v137 offset:1024
	ds_read_b128 v[182:185], v137 offset:2048
	ds_read_b128 v[186:189], v137 offset:3072
	ds_read_b128 v[190:193], v137 offset:4096
	ds_read_b128 v[194:197], v137 offset:5120
	ds_read_b128 v[198:201], v137 offset:6144
	ds_read_b128 v[202:205], v137 offset:7168
	buffer_load_dwordx4 v1, s[80:83], s45 offen lds
	s_mov_b32 m0, s33
	s_nop 0
	buffer_load_dwordx4 v1, s[80:83], s39 offen lds
	s_waitcnt vmcnt(8)
	s_waitcnt lgkmcnt(0)
	s_barrier
	s_setprio 1
	s_waitcnt lgkmcnt(6)
	v_mfma_scale_f32_16x16x128_f8f6f4 v[126:129], v[142:149], v[174:181], 0, v138, v138 op_sel:[0,1,0] op_sel_hi:[0,0,0]
	v_mfma_scale_f32_16x16x128_f8f6f4 v[122:125], v[150:157], v[174:181], 0, v138, v138 op_sel:[0,1,0] op_sel_hi:[0,0,0]
	s_waitcnt lgkmcnt(4)
	v_mfma_scale_f32_16x16x128_f8f6f4 v[118:121], v[142:149], v[182:189], 0, v138, v138 op_sel:[0,1,0] op_sel_hi:[0,0,0]
	v_mfma_scale_f32_16x16x128_f8f6f4 v[114:117], v[150:157], v[182:189], 0, v138, v138 op_sel:[0,1,0] op_sel_hi:[0,0,0]
	s_waitcnt lgkmcnt(2)
	v_mfma_scale_f32_16x16x128_f8f6f4 v[102:105], v[142:149], v[190:197], 0, v138, v138 op_sel:[0,1,0] op_sel_hi:[0,0,0]
	v_mfma_scale_f32_16x16x128_f8f6f4 v[98:101], v[150:157], v[190:197], 0, v138, v138 op_sel:[0,1,0] op_sel_hi:[0,0,0]
	s_waitcnt lgkmcnt(0)
	v_mfma_scale_f32_16x16x128_f8f6f4 v[206:209], v[142:149], v[198:205], 0, v138, v138 op_sel:[0,1,0] op_sel_hi:[0,0,0]
	v_mfma_scale_f32_16x16x128_f8f6f4 v[210:213], v[150:157], v[198:205], 0, v138, v138 op_sel:[0,1,0] op_sel_hi:[0,0,0]
	s_setprio 0
	s_setprio 1
	v_mfma_scale_f32_16x16x128_f8f6f4 v[110:113], v[158:165], v[174:181], 0, v138, v138 op_sel:[0,1,0] op_sel_hi:[0,0,0]
	v_mfma_scale_f32_16x16x128_f8f6f4 v[106:109], v[166:173], v[174:181], 0, v138, v138 op_sel:[0,1,0] op_sel_hi:[0,0,0]
	v_mfma_scale_f32_16x16x128_f8f6f4 v[174:177], v[158:165], v[182:189], 0, v138, v138 op_sel:[0,1,0] op_sel_hi:[0,0,0]
	v_mfma_scale_f32_16x16x128_f8f6f4 v[178:181], v[166:173], v[182:189], 0, v138, v138 op_sel:[0,1,0] op_sel_hi:[0,0,0]
	v_mfma_scale_f32_16x16x128_f8f6f4 v[182:185], v[158:165], v[190:197], 0, v138, v138 op_sel:[0,1,0] op_sel_hi:[0,0,0]
	v_mfma_scale_f32_16x16x128_f8f6f4 v[186:189], v[166:173], v[190:197], 0, v138, v138 op_sel:[0,1,0] op_sel_hi:[0,0,0]
	v_mfma_scale_f32_16x16x128_f8f6f4 v[190:193], v[158:165], v[198:205], 0, v138, v138 op_sel:[0,1,0] op_sel_hi:[0,0,0]
	v_mfma_scale_f32_16x16x128_f8f6f4 v[194:197], v[166:173], v[198:205], 0, v138, v138 op_sel:[0,1,0] op_sel_hi:[0,0,0]
	s_setprio 0
	s_barrier
	s_mov_b32 m0, s17
	s_nop 3
	ds_read_b128 v[66:69], v137 offset:16384
	ds_read_b128 v[70:73], v137 offset:17408
	ds_read_b128 v[74:77], v137 offset:18432
	ds_read_b128 v[78:81], v137 offset:19456
	ds_read_b128 v[82:85], v137 offset:20480
	ds_read_b128 v[86:89], v137 offset:21504
	ds_read_b128 v[90:93], v137 offset:22528
	ds_read_b128 v[94:97], v137 offset:23552
	buffer_load_dwordx4 v134, s[80:83], s44 offen lds
	s_add_i32 s45, s44, 0x20000
	s_mov_b32 m0, s18
	s_nop 0
	buffer_load_dwordx4 v134, s[80:83], s45 offen lds
	s_add_i32 s45, s44, 0x40000
	s_mov_b32 m0, s19
	s_nop 0
	buffer_load_dwordx4 v134, s[80:83], s45 offen lds
	s_add_i32 s45, s44, 0x60000
	s_mov_b32 m0, s20
	s_nop 0
	buffer_load_dwordx4 v134, s[80:83], s45 offen lds
	s_mov_b32 m0, s16
	s_add_i32 s45, s42, 0x20000
	buffer_load_dwordx4 v1, s[80:83], s42 offen lds
	s_mov_b32 m0, s21
	s_nop 0
	buffer_load_dwordx4 v1, s[80:83], s45 offen lds
	s_waitcnt vmcnt(8)
	s_waitcnt lgkmcnt(0)
	s_barrier
	s_setprio 1
	s_waitcnt lgkmcnt(6)
	v_mfma_scale_f32_16x16x128_f8f6f4 v[62:65], v[142:149], v[66:73], 0, v138, v138 op_sel:[0,1,0] op_sel_hi:[0,0,0]
	v_mfma_scale_f32_16x16x128_f8f6f4 v[58:61], v[150:157], v[66:73], 0, v138, v138 op_sel:[0,1,0] op_sel_hi:[0,0,0]
	s_waitcnt lgkmcnt(4)
	v_mfma_scale_f32_16x16x128_f8f6f4 v[54:57], v[142:149], v[74:81], 0, v138, v138 op_sel:[0,1,0] op_sel_hi:[0,0,0]
	v_mfma_scale_f32_16x16x128_f8f6f4 v[50:53], v[150:157], v[74:81], 0, v138, v138 op_sel:[0,1,0] op_sel_hi:[0,0,0]
	s_waitcnt lgkmcnt(2)
	v_mfma_scale_f32_16x16x128_f8f6f4 v[198:201], v[142:149], v[82:89], 0, v138, v138 op_sel:[0,1,0] op_sel_hi:[0,0,0]
	v_mfma_scale_f32_16x16x128_f8f6f4 v[202:205], v[150:157], v[82:89], 0, v138, v138 op_sel:[0,1,0] op_sel_hi:[0,0,0]
	s_waitcnt lgkmcnt(0)
	v_mfma_scale_f32_16x16x128_f8f6f4 v[214:217], v[142:149], v[90:97], 0, v138, v138 op_sel:[0,1,0] op_sel_hi:[0,0,0]
	v_mfma_scale_f32_16x16x128_f8f6f4 v[218:221], v[150:157], v[90:97], 0, v138, v138 op_sel:[0,1,0] op_sel_hi:[0,0,0]
	s_setprio 0
	s_setprio 1
	v_mfma_scale_f32_16x16x128_f8f6f4 v[222:225], v[158:165], v[66:73], 0, v138, v138 op_sel:[0,1,0] op_sel_hi:[0,0,0]
	v_mfma_scale_f32_16x16x128_f8f6f4 v[226:229], v[166:173], v[66:73], 0, v138, v138 op_sel:[0,1,0] op_sel_hi:[0,0,0]
	v_mfma_scale_f32_16x16x128_f8f6f4 v[230:233], v[158:165], v[74:81], 0, v138, v138 op_sel:[0,1,0] op_sel_hi:[0,0,0]
	v_mfma_scale_f32_16x16x128_f8f6f4 v[234:237], v[166:173], v[74:81], 0, v138, v138 op_sel:[0,1,0] op_sel_hi:[0,0,0]
	v_mfma_scale_f32_16x16x128_f8f6f4 v[238:241], v[158:165], v[82:89], 0, v138, v138 op_sel:[0,1,0] op_sel_hi:[0,0,0]
	v_mfma_scale_f32_16x16x128_f8f6f4 v[242:245], v[166:173], v[82:89], 0, v138, v138 op_sel:[0,1,0] op_sel_hi:[0,0,0]
	v_mfma_scale_f32_16x16x128_f8f6f4 v[246:249], v[158:165], v[90:97], 0, v138, v138 op_sel:[0,1,0] op_sel_hi:[0,0,0]
	v_mfma_scale_f32_16x16x128_f8f6f4 v[250:253], v[166:173], v[90:97], 0, v138, v138 op_sel:[0,1,0] op_sel_hi:[0,0,0]
	s_setprio 0
	s_barrier
; #define PG8_STAGE(bufoff, goff, voff) do { _Pragma("unroll") for (int _i = 0; _i < 2; ++_i) \
;         __builtin_amdgcn_raw_ptr_buffer_load_lds(rsrc, (PG8_LAS void*)(lds + (bufoff) + ldsw + _i * 8192), 16, (int)(voff), (int)((goff) + _i * p1##voff), 0, 0); } while (0)
; #define PG8_LDA(dst, b, h) do { _Pragma("unroll") for (int m = 0; m < 4; ++m) dst[m] = PG8_LD8(lds + PG8_SA(b, h) + aoff + m * 2048); } while (0)
; #define PG8_LDB(dst, b, h) do { _Pragma("unroll") for (int n = 0; n < 2; ++n) dst[n] = PG8_LD8(lds + PG8_SB(b, h) + boff + n * 2048); } while (0)
; #define PG8_WAIT_V(n) asm volatile("s_waitcnt vmcnt(" #n ")" ::: "memory")
; #define PG8_WAIT_L(n) asm volatile("s_waitcnt lgkmcnt(" #n ")" ::: "memory")
; #define PG8_BAR __builtin_amdgcn_s_barrier()
; #define PG8_SCHED __builtin_amdgcn_sched_barrier(0)
; template <class Epi, class Sched, bool ALIGN_EPI, bool F8 = false, int F8SC = F8_SCALES>
; __device__ __forceinline__ void gemm_phase(PG8_LAS unsigned char* lds, const __amdgpu_buffer_rsrc_t rsrc, const int lda, const int ldb, const int K, const Sched& S, const Epi& E) {
;     ...
;             PG8_LDB(B0, 1, 0); PG8_LDB(B1, 1, 1); PG8_SCHED; PG8_LDA(At, 1, 0); PG8_STAGE(PG8_SA(0, 1), a2 + hsA, voffA);
;             PG8_WAIT_V(8); PG8_WAIT_L(0); PG8_BAR; PG8_MMA(0, 0, At, B0); PG8_MMA(0, 1, At, B1); PG8_BAR; PG8_SCHED;
;             PG8_LDA(At, 1, 1); PG8_STAGE(PG8_SB(1, 0), b3, voffB); PG8_STAGE(PG8_SB(1, 1), b3 + hsB, voffB); PG8_STAGE(PG8_SA(1, 0), a3, voffA);
;             PG8_WAIT_V(8); PG8_WAIT_L(0); PG8_BAR; PG8_MMA(1, 0, At, B0); PG8_MMA(1, 1, At, B1); PG8_BAR; PG8_SCHED;
;         }
	s_nop 4
	ds_read_b128 v[2:5], v139
	ds_read_b128 v[6:9], v139 offset:1024
	ds_read_b128 v[10:13], v139 offset:2048
	ds_read_b128 v[14:17], v139 offset:3072
	ds_read_b128 v[142:145], v140
	ds_read_b128 v[146:149], v140 offset:1024
	ds_read_b128 v[150:153], v140 offset:2048
	ds_read_b128 v[154:157], v140 offset:3072
	s_mov_b32 m0, s22
	s_add_i32 s45, s42, 0x40000
	ds_read_b128 v[18:21], v137 offset:32768
	ds_read_b128 v[22:25], v137 offset:33792
	ds_read_b128 v[26:29], v137 offset:34816
	ds_read_b128 v[30:33], v137 offset:35840
	ds_read_b128 v[34:37], v137 offset:36864
	ds_read_b128 v[38:41], v137 offset:37888
	ds_read_b128 v[42:45], v137 offset:38912
	ds_read_b128 v[46:49], v137 offset:39936
	buffer_load_dwordx4 v1, s[80:83], s45 offen lds
	s_add_i32 s45, s42, 0x60000
	s_mov_b32 m0, s23
	s_nop 0
	buffer_load_dwordx4 v1, s[80:83], s45 offen lds
	s_waitcnt vmcnt(8)
	s_waitcnt lgkmcnt(0)
	s_barrier
	s_setprio 1
	s_waitcnt lgkmcnt(6)
	v_mfma_scale_f32_16x16x128_f8f6f4 v[126:129], v[2:9], v[18:25], v[126:129], v138, v138 op_sel:[0,1,0] op_sel_hi:[0,0,0]
	v_mfma_scale_f32_16x16x128_f8f6f4 v[122:125], v[10:17], v[18:25], v[122:125], v138, v138 op_sel:[0,1,0] op_sel_hi:[0,0,0]
	s_waitcnt lgkmcnt(4)
	v_mfma_scale_f32_16x16x128_f8f6f4 v[118:121], v[2:9], v[26:33], v[118:121], v138, v138 op_sel:[0,1,0] op_sel_hi:[0,0,0]
	v_mfma_scale_f32_16x16x128_f8f6f4 v[114:117], v[10:17], v[26:33], v[114:117], v138, v138 op_sel:[0,1,0] op_sel_hi:[0,0,0]
	s_waitcnt lgkmcnt(2)
	v_mfma_scale_f32_16x16x128_f8f6f4 v[102:105], v[2:9], v[34:41], v[102:105], v138, v138 op_sel:[0,1,0] op_sel_hi:[0,0,0]
	v_mfma_scale_f32_16x16x128_f8f6f4 v[98:101], v[10:17], v[34:41], v[98:101], v138, v138 op_sel:[0,1,0] op_sel_hi:[0,0,0]
	s_waitcnt lgkmcnt(0)
	v_mfma_scale_f32_16x16x128_f8f6f4 v[86:89], v[2:9], v[42:49], v[206:209], v138, v138 op_sel:[0,1,0] op_sel_hi:[0,0,0]
	v_mfma_scale_f32_16x16x128_f8f6f4 v[82:85], v[10:17], v[42:49], v[210:213], v138, v138 op_sel:[0,1,0] op_sel_hi:[0,0,0]
	s_setprio 0
	s_setprio 1
	v_mfma_scale_f32_16x16x128_f8f6f4 v[110:113], v[142:149], v[18:25], v[110:113], v138, v138 op_sel:[0,1,0] op_sel_hi:[0,0,0]
	v_mfma_scale_f32_16x16x128_f8f6f4 v[106:109], v[150:157], v[18:25], v[106:109], v138, v138 op_sel:[0,1,0] op_sel_hi:[0,0,0]
	v_mfma_scale_f32_16x16x128_f8f6f4 v[94:97], v[142:149], v[26:33], v[174:177], v138, v138 op_sel:[0,1,0] op_sel_hi:[0,0,0]
	v_mfma_scale_f32_16x16x128_f8f6f4 v[90:93], v[150:157], v[26:33], v[178:181], v138, v138 op_sel:[0,1,0] op_sel_hi:[0,0,0]
	v_mfma_scale_f32_16x16x128_f8f6f4 v[78:81], v[142:149], v[34:41], v[182:185], v138, v138 op_sel:[0,1,0] op_sel_hi:[0,0,0]
	v_mfma_scale_f32_16x16x128_f8f6f4 v[74:77], v[150:157], v[34:41], v[186:189], v138, v138 op_sel:[0,1,0] op_sel_hi:[0,0,0]
	v_mfma_scale_f32_16x16x128_f8f6f4 v[70:73], v[142:149], v[42:49], v[190:193], v138, v138 op_sel:[0,1,0] op_sel_hi:[0,0,0]
	v_mfma_scale_f32_16x16x128_f8f6f4 v[66:69], v[150:157], v[42:49], v[194:197], v138, v138 op_sel:[0,1,0] op_sel_hi:[0,0,0]
	s_setprio 0
	s_barrier
	s_mov_b32 m0, s25
	s_add_i32 s45, s44, 0x80
	ds_read_b128 v[26:29], v137 offset:49152
	ds_read_b128 v[30:33], v137 offset:50176
	ds_read_b128 v[158:161], v137 offset:51200
	ds_read_b128 v[162:165], v137 offset:52224
	ds_read_b128 v[166:169], v137 offset:53248
	ds_read_b128 v[170:173], v137 offset:54272
	ds_read_b128 v[174:177], v137 offset:55296
	ds_read_b128 v[178:181], v137 offset:56320
	buffer_load_dwordx4 v134, s[80:83], s45 offen lds
	s_add_i32 s45, s44, 0x20080
	s_mov_b32 m0, s26
	s_add_i32 s42, s42, 0x20080
	buffer_load_dwordx4 v134, s[80:83], s45 offen lds
	s_add_i32 s45, s44, 0x40080
	s_mov_b32 m0, s29
	s_add_i32 s44, s44, 0x60080
	buffer_load_dwordx4 v134, s[80:83], s45 offen lds
	s_mov_b32 m0, s30
	s_nop 0
	buffer_load_dwordx4 v134, s[80:83], s44 offen lds
	s_mov_b32 m0, s27
	s_nop 0
	buffer_load_dwordx4 v1, s[80:83], s43 offen lds
	s_mov_b32 m0, s28
	s_nop 0
	buffer_load_dwordx4 v1, s[80:83], s42 offen lds
	s_waitcnt vmcnt(8)
	s_waitcnt lgkmcnt(0)
	s_barrier
	s_setprio 1
	s_waitcnt lgkmcnt(6)
	v_mfma_scale_f32_16x16x128_f8f6f4 v[62:65], v[2:9], v[26:33], v[62:65], v138, v138 op_sel:[0,1,0] op_sel_hi:[0,0,0]
	v_mfma_scale_f32_16x16x128_f8f6f4 v[58:61], v[10:17], v[26:33], v[58:61], v138, v138 op_sel:[0,1,0] op_sel_hi:[0,0,0]
	s_waitcnt lgkmcnt(4)
	v_mfma_scale_f32_16x16x128_f8f6f4 v[54:57], v[2:9], v[158:165], v[54:57], v138, v138 op_sel:[0,1,0] op_sel_hi:[0,0,0]
	v_mfma_scale_f32_16x16x128_f8f6f4 v[50:53], v[10:17], v[158:165], v[50:53], v138, v138 op_sel:[0,1,0] op_sel_hi:[0,0,0]
	s_waitcnt lgkmcnt(2)
	v_mfma_scale_f32_16x16x128_f8f6f4 v[38:41], v[2:9], v[166:173], v[198:201], v138, v138 op_sel:[0,1,0] op_sel_hi:[0,0,0]
	v_mfma_scale_f32_16x16x128_f8f6f4 v[34:37], v[10:17], v[166:173], v[202:205], v138, v138 op_sel:[0,1,0] op_sel_hi:[0,0,0]
	s_waitcnt lgkmcnt(0)
	v_mfma_scale_f32_16x16x128_f8f6f4 v[22:25], v[2:9], v[174:181], v[214:217], v138, v138 op_sel:[0,1,0] op_sel_hi:[0,0,0]
	v_mfma_scale_f32_16x16x128_f8f6f4 v[18:21], v[10:17], v[174:181], v[218:221], v138, v138 op_sel:[0,1,0] op_sel_hi:[0,0,0]
	s_setprio 0
	s_setprio 1
	v_mfma_scale_f32_16x16x128_f8f6f4 v[46:49], v[142:149], v[26:33], v[222:225], v138, v138 op_sel:[0,1,0] op_sel_hi:[0,0,0]
	v_mfma_scale_f32_16x16x128_f8f6f4 v[42:45], v[150:157], v[26:33], v[226:229], v138, v138 op_sel:[0,1,0] op_sel_hi:[0,0,0]
	v_mfma_scale_f32_16x16x128_f8f6f4 v[30:33], v[142:149], v[158:165], v[230:233], v138, v138 op_sel:[0,1,0] op_sel_hi:[0,0,0]
	v_mfma_scale_f32_16x16x128_f8f6f4 v[26:29], v[150:157], v[158:165], v[234:237], v138, v138 op_sel:[0,1,0] op_sel_hi:[0,0,0]
	v_mfma_scale_f32_16x16x128_f8f6f4 v[14:17], v[142:149], v[166:173], v[238:241], v138, v138 op_sel:[0,1,0] op_sel_hi:[0,0,0]
	v_mfma_scale_f32_16x16x128_f8f6f4 v[10:13], v[150:157], v[166:173], v[242:245], v138, v138 op_sel:[0,1,0] op_sel_hi:[0,0,0]
	v_mfma_scale_f32_16x16x128_f8f6f4 v[6:9], v[142:149], v[174:181], v[246:249], v138, v138 op_sel:[0,1,0] op_sel_hi:[0,0,0]
	v_mfma_scale_f32_16x16x128_f8f6f4 v[2:5], v[150:157], v[174:181], v[250:253], v138, v138 op_sel:[0,1,0] op_sel_hi:[0,0,0]
	s_setprio 0
	s_barrier
	s_add_i32 s41, s41, 2
	s_addk_i32 s39, 0x100
	s_addk_i32 s40, 0x100
	s_cmp_gt_u32 s41, 13
	s_cbranch_scc0 .LBB0_791
	s_branch .Lpeel_after_791

; #define PG8_BAR __builtin_amdgcn_s_barrier()
; template <class Epi, class Sched, bool ALIGN_EPI, bool F8 = false, int F8SC = F8_SCALES>
; __device__ __forceinline__ void gemm_phase(PG8_LAS unsigned char* lds, const __amdgpu_buffer_rsrc_t rsrc, const int lda, const int ldb, const int K, const Sched& S, const Epi& E) {
;     ...
;         if constexpr (ALIGN_EPI) { if (wr == 0) PG8_BAR; }
.Lpeel_after_791:
	s_and_b64 vcc, exec, s[10:11]
	s_cbranch_vccz .LBB0_794
	s_barrier

;     __device__ __forceinline__ bool next(int i, Unit& u) const { u.aux = 0; return t.map(i, u.pm, u.pn); }
;     __device__ __forceinline__ bool next(int i, Unit& u) const { u.aux = i & 1; return t.map(i >> 1, u.pm, u.pn); }
; #define PG8_WAIT_V(n) asm volatile("s_waitcnt vmcnt(" #n ")" ::: "memory")
; #define PG8_BAR __builtin_amdgcn_s_barrier()
; template <class Epi, class Sched, bool ALIGN_EPI, bool F8 = false, int F8SC = F8_SCALES>
; __device__ __forceinline__ void gemm_phase(PG8_LAS unsigned char* lds, const __amdgpu_buffer_rsrc_t rsrc, const int lda, const int ldb, const int K, const Sched& S, const Epi& E) {
;     ...
;     Unit cur, nxt; int ui = 0;
;     if (!S.next(0, cur)) return;
;     f32x4 acc[2][2][4][2];
;     PG8_ZERO();
;     i32x8 At[4], B0[2], B1[2];
;     unsigned cA, cB; S.bases(cur, cA, cB); cA = __builtin_amdgcn_readfirstlane(cA); cB = __builtin_amdgcn_readfirstlane(cB);
;     PG8_STAGE(PG8_SB(0, 0), cB, voffB); PG8_STAGE(PG8_SB(0, 1), cB + hsB, voffB); PG8_STAGE(PG8_SA(0, 0), cA, voffA); PG8_STAGE(PG8_SA(0, 1), cA + hsA, voffA);
;     if (wr == 1) PG8_BAR;
;     PG8_WAIT_V(2); PG8_BAR;
;     PG8_STAGE(PG8_SB(1, 0), cB + kstep, voffB); PG8_STAGE(PG8_SA(1, 0), cA + kstep, voffA); PG8_STAGE(PG8_SB(1, 1), cB + hsB + kstep, voffB);
;     PG8_WAIT_V(6); PG8_BAR;
;     for (;;) {
;         const bool has_next = S.next(ui + 1, nxt);
;         unsigned nA = cA, nB = cB; if (has_next) { S.bases(nxt, nA, nB); nA = __builtin_amdgcn_readfirstlane(nA); nB = __builtin_amdgcn_readfirstlane(nB); }
; #pragma unroll 1
;         for (int t = 0; t < nt; t += 2) {
;             const bool last = (t == nt - 2);
;             const unsigned a1 = cA + (unsigned)(t + 1) * kstep;
;             const unsigned a2 = last ? nA : cA + (unsigned)(t + 2) * kstep, b2 = last ? nB : cB + (unsigned)(t + 2) * kstep;
;             const unsigned a3 = a2 + kstep, b3 = b2 + kstep;
;             PG8_LDB(B0, 0, 0); PG8_LDB(B1, 0, 1); PG8_SCHED; PG8_LDA(At, 0, 0); PG8_STAGE(PG8_SA(1, 1), a1 + hsA, voffA);
;             PG8_WAIT_V(8); PG8_WAIT_L(0); PG8_BAR; PG8_MMA(0, 0, At, B0); PG8_MMA(0, 1, At, B1); PG8_BAR; PG8_SCHED;
;             PG8_LDA(At, 0, 1); PG8_STAGE(PG8_SB(0, 0), b2, voffB); PG8_STAGE(PG8_SB(0, 1), b2 + hsB, voffB); PG8_STAGE(PG8_SA(0, 0), a2, voffA);
;             PG8_WAIT_V(8); PG8_WAIT_L(0); PG8_BAR; PG8_MMA(1, 0, At, B0); PG8_MMA(1, 1, At, B1); PG8_BAR; PG8_SCHED;
.LBB0_1447:
	s_add_i32 s44, s44, 0x60080
	s_addk_i32 s45, 0x100
	s_mov_b32 s46, -2
	ds_read_b128 v[142:145], v135
	ds_read_b128 v[146:149], v135 offset:1024
	ds_read_b128 v[150:153], v135 offset:2048
	ds_read_b128 v[154:157], v135 offset:3072
	ds_read_b128 v[158:161], v136
	ds_read_b128 v[162:165], v136 offset:1024
	ds_read_b128 v[166:169], v136 offset:2048
	ds_read_b128 v[170:173], v136 offset:3072
	s_add_i32 s47, s44, 0xfffa0080
	s_cmp_eq_u32 s46, 12
	s_cselect_b32 s47, s4, s47
	s_cselect_b32 s49, s5, s45
	s_add_i32 s48, s47, 0x80
	s_add_i32 s50, s44, 0xfffe0000
	s_mov_b32 s80, s96
	s_mov_b32 m0, s33
	ds_read_b128 v[174:177], v137
	ds_read_b128 v[178:181], v137 offset:1024
	ds_read_b128 v[182:185], v137 offset:2048
	ds_read_b128 v[186:189], v137 offset:3072
	ds_read_b128 v[190:193], v137 offset:4096
	ds_read_b128 v[194:197], v137 offset:5120
	ds_read_b128 v[198:201], v137 offset:6144
	ds_read_b128 v[202:205], v137 offset:7168
	buffer_load_dwordx4 v1, s[80:83], s50 offen lds
	s_mov_b32 m0, s34
	s_nop 0
	buffer_load_dwordx4 v1, s[80:83], s44 offen lds
	s_waitcnt vmcnt(8)
	s_waitcnt lgkmcnt(0)
	s_barrier
	s_setprio 1
	s_waitcnt lgkmcnt(6)
	v_mfma_scale_f32_16x16x128_f8f6f4 v[126:129], v[142:149], v[174:181], 0, v138, v138 op_sel:[0,1,0] op_sel_hi:[0,0,0]
	v_mfma_scale_f32_16x16x128_f8f6f4 v[122:125], v[150:157], v[174:181], 0, v138, v138 op_sel:[0,1,0] op_sel_hi:[0,0,0]
	s_waitcnt lgkmcnt(4)
	v_mfma_scale_f32_16x16x128_f8f6f4 v[118:121], v[142:149], v[182:189], 0, v138, v138 op_sel:[0,1,0] op_sel_hi:[0,0,0]
	v_mfma_scale_f32_16x16x128_f8f6f4 v[114:117], v[150:157], v[182:189], 0, v138, v138 op_sel:[0,1,0] op_sel_hi:[0,0,0]
	s_waitcnt lgkmcnt(2)
	v_mfma_scale_f32_16x16x128_f8f6f4 v[102:105], v[142:149], v[190:197], 0, v138, v138 op_sel:[0,1,0] op_sel_hi:[0,0,0]
	v_mfma_scale_f32_16x16x128_f8f6f4 v[98:101], v[150:157], v[190:197], 0, v138, v138 op_sel:[0,1,0] op_sel_hi:[0,0,0]
	s_waitcnt lgkmcnt(0)
	v_mfma_scale_f32_16x16x128_f8f6f4 v[206:209], v[142:149], v[198:205], 0, v138, v138 op_sel:[0,1,0] op_sel_hi:[0,0,0]
	v_mfma_scale_f32_16x16x128_f8f6f4 v[210:213], v[150:157], v[198:205], 0, v138, v138 op_sel:[0,1,0] op_sel_hi:[0,0,0]
	s_setprio 0
	s_setprio 1
	v_mfma_scale_f32_16x16x128_f8f6f4 v[110:113], v[158:165], v[174:181], 0, v138, v138 op_sel:[0,1,0] op_sel_hi:[0,0,0]
	v_mfma_scale_f32_16x16x128_f8f6f4 v[106:109], v[166:173], v[174:181], 0, v138, v138 op_sel:[0,1,0] op_sel_hi:[0,0,0]
	v_mfma_scale_f32_16x16x128_f8f6f4 v[174:177], v[158:165], v[182:189], 0, v138, v138 op_sel:[0,1,0] op_sel_hi:[0,0,0]
	v_mfma_scale_f32_16x16x128_f8f6f4 v[178:181], v[166:173], v[182:189], 0, v138, v138 op_sel:[0,1,0] op_sel_hi:[0,0,0]
	v_mfma_scale_f32_16x16x128_f8f6f4 v[182:185], v[158:165], v[190:197], 0, v138, v138 op_sel:[0,1,0] op_sel_hi:[0,0,0]
	v_mfma_scale_f32_16x16x128_f8f6f4 v[186:189], v[166:173], v[190:197], 0, v138, v138 op_sel:[0,1,0] op_sel_hi:[0,0,0]
	v_mfma_scale_f32_16x16x128_f8f6f4 v[190:193], v[158:165], v[198:205], 0, v138, v138 op_sel:[0,1,0] op_sel_hi:[0,0,0]
	v_mfma_scale_f32_16x16x128_f8f6f4 v[194:197], v[166:173], v[198:205], 0, v138, v138 op_sel:[0,1,0] op_sel_hi:[0,0,0]
	s_setprio 0
	s_barrier
	s_mov_b32 m0, s18
	s_nop 3
	ds_read_b128 v[66:69], v137 offset:16384
	ds_read_b128 v[70:73], v137 offset:17408
	ds_read_b128 v[74:77], v137 offset:18432
	ds_read_b128 v[78:81], v137 offset:19456
	ds_read_b128 v[82:85], v137 offset:20480
	ds_read_b128 v[86:89], v137 offset:21504
	ds_read_b128 v[90:93], v137 offset:22528
	ds_read_b128 v[94:97], v137 offset:23552
	buffer_load_dwordx4 v134, s[80:83], s49 offen lds
	s_add_i32 s50, s49, 0x20000
	s_mov_b32 m0, s19
	s_nop 0
	buffer_load_dwordx4 v134, s[80:83], s50 offen lds
	s_add_i32 s50, s49, 0x40000
	s_mov_b32 m0, s20
	s_nop 0
	buffer_load_dwordx4 v134, s[80:83], s50 offen lds
	s_add_i32 s50, s49, 0x60000
	s_mov_b32 m0, s21
	s_nop 0
	buffer_load_dwordx4 v134, s[80:83], s50 offen lds
	s_mov_b32 m0, s9
	s_add_i32 s50, s47, 0x20000
	buffer_load_dwordx4 v1, s[80:83], s47 offen lds
	s_mov_b32 m0, s22
	s_nop 0
	buffer_load_dwordx4 v1, s[80:83], s50 offen lds
	s_waitcnt vmcnt(8)
	s_waitcnt lgkmcnt(0)
	s_barrier
	s_setprio 1
	s_waitcnt lgkmcnt(6)
	v_mfma_scale_f32_16x16x128_f8f6f4 v[62:65], v[142:149], v[66:73], 0, v138, v138 op_sel:[0,1,0] op_sel_hi:[0,0,0]
	v_mfma_scale_f32_16x16x128_f8f6f4 v[58:61], v[150:157], v[66:73], 0, v138, v138 op_sel:[0,1,0] op_sel_hi:[0,0,0]
	s_waitcnt lgkmcnt(4)
	v_mfma_scale_f32_16x16x128_f8f6f4 v[54:57], v[142:149], v[74:81], 0, v138, v138 op_sel:[0,1,0] op_sel_hi:[0,0,0]
	v_mfma_scale_f32_16x16x128_f8f6f4 v[50:53], v[150:157], v[74:81], 0, v138, v138 op_sel:[0,1,0] op_sel_hi:[0,0,0]
	s_waitcnt lgkmcnt(2)
	v_mfma_scale_f32_16x16x128_f8f6f4 v[198:201], v[142:149], v[82:89], 0, v138, v138 op_sel:[0,1,0] op_sel_hi:[0,0,0]
	v_mfma_scale_f32_16x16x128_f8f6f4 v[202:205], v[150:157], v[82:89], 0, v138, v138 op_sel:[0,1,0] op_sel_hi:[0,0,0]
	s_waitcnt lgkmcnt(0)
	v_mfma_scale_f32_16x16x128_f8f6f4 v[214:217], v[142:149], v[90:97], 0, v138, v138 op_sel:[0,1,0] op_sel_hi:[0,0,0]
	v_mfma_scale_f32_16x16x128_f8f6f4 v[218:221], v[150:157], v[90:97], 0, v138, v138 op_sel:[0,1,0] op_sel_hi:[0,0,0]
	s_setprio 0
	s_setprio 1
	v_mfma_scale_f32_16x16x128_f8f6f4 v[222:225], v[158:165], v[66:73], 0, v138, v138 op_sel:[0,1,0] op_sel_hi:[0,0,0]
	v_mfma_scale_f32_16x16x128_f8f6f4 v[226:229], v[166:173], v[66:73], 0, v138, v138 op_sel:[0,1,0] op_sel_hi:[0,0,0]
	v_mfma_scale_f32_16x16x128_f8f6f4 v[230:233], v[158:165], v[74:81], 0, v138, v138 op_sel:[0,1,0] op_sel_hi:[0,0,0]
	v_mfma_scale_f32_16x16x128_f8f6f4 v[234:237], v[166:173], v[74:81], 0, v138, v138 op_sel:[0,1,0] op_sel_hi:[0,0,0]
	v_mfma_scale_f32_16x16x128_f8f6f4 v[238:241], v[158:165], v[82:89], 0, v138, v138 op_sel:[0,1,0] op_sel_hi:[0,0,0]
	v_mfma_scale_f32_16x16x128_f8f6f4 v[242:245], v[166:173], v[82:89], 0, v138, v138 op_sel:[0,1,0] op_sel_hi:[0,0,0]
	v_mfma_scale_f32_16x16x128_f8f6f4 v[246:249], v[158:165], v[90:97], 0, v138, v138 op_sel:[0,1,0] op_sel_hi:[0,0,0]
	v_mfma_scale_f32_16x16x128_f8f6f4 v[250:253], v[166:173], v[90:97], 0, v138, v138 op_sel:[0,1,0] op_sel_hi:[0,0,0]
	s_setprio 0
	s_barrier
; #define PG8_STAGE(bufoff, goff, voff) do { _Pragma("unroll") for (int _i = 0; _i < 2; ++_i) \
;         __builtin_amdgcn_raw_ptr_buffer_load_lds(rsrc, (PG8_LAS void*)(lds + (bufoff) + ldsw + _i * 8192), 16, (int)(voff), (int)((goff) + _i * p1##voff), 0, 0); } while (0)
; #define PG8_LDA(dst, b, h) do { _Pragma("unroll") for (int m = 0; m < 4; ++m) dst[m] = PG8_LD8(lds + PG8_SA(b, h) + aoff + m * 2048); } while (0)
; #define PG8_LDB(dst, b, h) do { _Pragma("unroll") for (int n = 0; n < 2; ++n) dst[n] = PG8_LD8(lds + PG8_SB(b, h) + boff + n * 2048); } while (0)
; #define PG8_WAIT_V(n) asm volatile("s_waitcnt vmcnt(" #n ")" ::: "memory")
; #define PG8_WAIT_L(n) asm volatile("s_waitcnt lgkmcnt(" #n ")" ::: "memory")
; #define PG8_BAR __builtin_amdgcn_s_barrier()
; #define PG8_SCHED __builtin_amdgcn_sched_barrier(0)
; template <class Epi, class Sched, bool ALIGN_EPI, bool F8 = false, int F8SC = F8_SCALES>
; __device__ __forceinline__ void gemm_phase(PG8_LAS unsigned char* lds, const __amdgpu_buffer_rsrc_t rsrc, const int lda, const int ldb, const int K, const Sched& S, const Epi& E) {
;     ...
;             PG8_LDB(B0, 1, 0); PG8_LDB(B1, 1, 1); PG8_SCHED; PG8_LDA(At, 1, 0); PG8_STAGE(PG8_SA(0, 1), a2 + hsA, voffA);
;             PG8_WAIT_V(8); PG8_WAIT_L(0); PG8_BAR; PG8_MMA(0, 0, At, B0); PG8_MMA(0, 1, At, B1); PG8_BAR; PG8_SCHED;
;             PG8_LDA(At, 1, 1); PG8_STAGE(PG8_SB(1, 0), b3, voffB); PG8_STAGE(PG8_SB(1, 1), b3 + hsB, voffB); PG8_STAGE(PG8_SA(1, 0), a3, voffA);
;             PG8_WAIT_V(8); PG8_WAIT_L(0); PG8_BAR; PG8_MMA(1, 0, At, B0); PG8_MMA(1, 1, At, B1); PG8_BAR; PG8_SCHED;
;         }
	s_nop 4
	ds_read_b128 v[2:5], v139
	ds_read_b128 v[6:9], v139 offset:1024
	ds_read_b128 v[10:13], v139 offset:2048
	ds_read_b128 v[14:17], v139 offset:3072
	ds_read_b128 v[142:145], v140
	ds_read_b128 v[146:149], v140 offset:1024
	ds_read_b128 v[150:153], v140 offset:2048
	ds_read_b128 v[154:157], v140 offset:3072
	s_mov_b32 m0, s23
	s_add_i32 s50, s47, 0x40000
	ds_read_b128 v[18:21], v137 offset:32768
	ds_read_b128 v[22:25], v137 offset:33792
	ds_read_b128 v[26:29], v137 offset:34816
	ds_read_b128 v[30:33], v137 offset:35840
	ds_read_b128 v[34:37], v137 offset:36864
	ds_read_b128 v[38:41], v137 offset:37888
	ds_read_b128 v[42:45], v137 offset:38912
	ds_read_b128 v[46:49], v137 offset:39936
	buffer_load_dwordx4 v1, s[80:83], s50 offen lds
	s_add_i32 s50, s47, 0x60000
	s_mov_b32 m0, s24
	s_nop 0
	buffer_load_dwordx4 v1, s[80:83], s50 offen lds
	s_waitcnt vmcnt(8)
	s_waitcnt lgkmcnt(0)
	s_barrier
	s_setprio 1
	s_waitcnt lgkmcnt(6)
	v_mfma_scale_f32_16x16x128_f8f6f4 v[126:129], v[2:9], v[18:25], v[126:129], v138, v138 op_sel:[0,1,0] op_sel_hi:[0,0,0]
	v_mfma_scale_f32_16x16x128_f8f6f4 v[122:125], v[10:17], v[18:25], v[122:125], v138, v138 op_sel:[0,1,0] op_sel_hi:[0,0,0]
	s_waitcnt lgkmcnt(4)
	v_mfma_scale_f32_16x16x128_f8f6f4 v[118:121], v[2:9], v[26:33], v[118:121], v138, v138 op_sel:[0,1,0] op_sel_hi:[0,0,0]
	v_mfma_scale_f32_16x16x128_f8f6f4 v[114:117], v[10:17], v[26:33], v[114:117], v138, v138 op_sel:[0,1,0] op_sel_hi:[0,0,0]
	s_waitcnt lgkmcnt(2)
	v_mfma_scale_f32_16x16x128_f8f6f4 v[102:105], v[2:9], v[34:41], v[102:105], v138, v138 op_sel:[0,1,0] op_sel_hi:[0,0,0]
	v_mfma_scale_f32_16x16x128_f8f6f4 v[98:101], v[10:17], v[34:41], v[98:101], v138, v138 op_sel:[0,1,0] op_sel_hi:[0,0,0]
	s_waitcnt lgkmcnt(0)
	v_mfma_scale_f32_16x16x128_f8f6f4 v[86:89], v[2:9], v[42:49], v[206:209], v138, v138 op_sel:[0,1,0] op_sel_hi:[0,0,0]
	v_mfma_scale_f32_16x16x128_f8f6f4 v[82:85], v[10:17], v[42:49], v[210:213], v138, v138 op_sel:[0,1,0] op_sel_hi:[0,0,0]
	s_setprio 0
	s_setprio 1
	v_mfma_scale_f32_16x16x128_f8f6f4 v[110:113], v[142:149], v[18:25], v[110:113], v138, v138 op_sel:[0,1,0] op_sel_hi:[0,0,0]
	v_mfma_scale_f32_16x16x128_f8f6f4 v[106:109], v[150:157], v[18:25], v[106:109], v138, v138 op_sel:[0,1,0] op_sel_hi:[0,0,0]
	v_mfma_scale_f32_16x16x128_f8f6f4 v[94:97], v[142:149], v[26:33], v[174:177], v138, v138 op_sel:[0,1,0] op_sel_hi:[0,0,0]
	v_mfma_scale_f32_16x16x128_f8f6f4 v[90:93], v[150:157], v[26:33], v[178:181], v138, v138 op_sel:[0,1,0] op_sel_hi:[0,0,0]
	v_mfma_scale_f32_16x16x128_f8f6f4 v[78:81], v[142:149], v[34:41], v[182:185], v138, v138 op_sel:[0,1,0] op_sel_hi:[0,0,0]
	v_mfma_scale_f32_16x16x128_f8f6f4 v[74:77], v[150:157], v[34:41], v[186:189], v138, v138 op_sel:[0,1,0] op_sel_hi:[0,0,0]
	v_mfma_scale_f32_16x16x128_f8f6f4 v[70:73], v[142:149], v[42:49], v[190:193], v138, v138 op_sel:[0,1,0] op_sel_hi:[0,0,0]
	v_mfma_scale_f32_16x16x128_f8f6f4 v[66:69], v[150:157], v[42:49], v[194:197], v138, v138 op_sel:[0,1,0] op_sel_hi:[0,0,0]
	s_setprio 0
	s_barrier
	s_mov_b32 m0, s26
	s_add_i32 s50, s49, 0x80
	ds_read_b128 v[26:29], v137 offset:49152
	ds_read_b128 v[30:33], v137 offset:50176
	ds_read_b128 v[158:161], v137 offset:51200
	ds_read_b128 v[162:165], v137 offset:52224
	ds_read_b128 v[166:169], v137 offset:53248
	ds_read_b128 v[170:173], v137 offset:54272
	ds_read_b128 v[174:177], v137 offset:55296
	ds_read_b128 v[178:181], v137 offset:56320
	buffer_load_dwordx4 v134, s[80:83], s50 offen lds
	s_add_i32 s50, s49, 0x20080
	s_mov_b32 m0, s27
	s_add_i32 s47, s47, 0x20080
	buffer_load_dwordx4 v134, s[80:83], s50 offen lds
	s_add_i32 s50, s49, 0x40080
	s_mov_b32 m0, s30
	s_add_i32 s49, s49, 0x60080
	buffer_load_dwordx4 v134, s[80:83], s50 offen lds
	s_mov_b32 m0, s31
	s_nop 0
	buffer_load_dwordx4 v134, s[80:83], s49 offen lds
	s_mov_b32 m0, s28
	s_nop 0
	buffer_load_dwordx4 v1, s[80:83], s48 offen lds
	s_mov_b32 m0, s29
	s_nop 0
	buffer_load_dwordx4 v1, s[80:83], s47 offen lds
	s_waitcnt vmcnt(8)
	s_waitcnt lgkmcnt(0)
	s_barrier
	s_setprio 1
	s_waitcnt lgkmcnt(6)
	v_mfma_scale_f32_16x16x128_f8f6f4 v[62:65], v[2:9], v[26:33], v[62:65], v138, v138 op_sel:[0,1,0] op_sel_hi:[0,0,0]
	v_mfma_scale_f32_16x16x128_f8f6f4 v[58:61], v[10:17], v[26:33], v[58:61], v138, v138 op_sel:[0,1,0] op_sel_hi:[0,0,0]
	s_waitcnt lgkmcnt(4)
	v_mfma_scale_f32_16x16x128_f8f6f4 v[54:57], v[2:9], v[158:165], v[54:57], v138, v138 op_sel:[0,1,0] op_sel_hi:[0,0,0]
	v_mfma_scale_f32_16x16x128_f8f6f4 v[50:53], v[10:17], v[158:165], v[50:53], v138, v138 op_sel:[0,1,0] op_sel_hi:[0,0,0]
	s_waitcnt lgkmcnt(2)
	v_mfma_scale_f32_16x16x128_f8f6f4 v[38:41], v[2:9], v[166:173], v[198:201], v138, v138 op_sel:[0,1,0] op_sel_hi:[0,0,0]
	v_mfma_scale_f32_16x16x128_f8f6f4 v[34:37], v[10:17], v[166:173], v[202:205], v138, v138 op_sel:[0,1,0] op_sel_hi:[0,0,0]
	s_waitcnt lgkmcnt(0)
	v_mfma_scale_f32_16x16x128_f8f6f4 v[22:25], v[2:9], v[174:181], v[214:217], v138, v138 op_sel:[0,1,0] op_sel_hi:[0,0,0]
	v_mfma_scale_f32_16x16x128_f8f6f4 v[18:21], v[10:17], v[174:181], v[218:221], v138, v138 op_sel:[0,1,0] op_sel_hi:[0,0,0]
	s_setprio 0
	s_setprio 1
	v_mfma_scale_f32_16x16x128_f8f6f4 v[46:49], v[142:149], v[26:33], v[222:225], v138, v138 op_sel:[0,1,0] op_sel_hi:[0,0,0]
	v_mfma_scale_f32_16x16x128_f8f6f4 v[42:45], v[150:157], v[26:33], v[226:229], v138, v138 op_sel:[0,1,0] op_sel_hi:[0,0,0]
	v_mfma_scale_f32_16x16x128_f8f6f4 v[30:33], v[142:149], v[158:165], v[230:233], v138, v138 op_sel:[0,1,0] op_sel_hi:[0,0,0]
	v_mfma_scale_f32_16x16x128_f8f6f4 v[26:29], v[150:157], v[158:165], v[234:237], v138, v138 op_sel:[0,1,0] op_sel_hi:[0,0,0]
	v_mfma_scale_f32_16x16x128_f8f6f4 v[14:17], v[142:149], v[166:173], v[238:241], v138, v138 op_sel:[0,1,0] op_sel_hi:[0,0,0]
	v_mfma_scale_f32_16x16x128_f8f6f4 v[10:13], v[150:157], v[166:173], v[242:245], v138, v138 op_sel:[0,1,0] op_sel_hi:[0,0,0]
	v_mfma_scale_f32_16x16x128_f8f6f4 v[6:9], v[142:149], v[174:181], v[246:249], v138, v138 op_sel:[0,1,0] op_sel_hi:[0,0,0]
	v_mfma_scale_f32_16x16x128_f8f6f4 v[2:5], v[150:157], v[174:181], v[250:253], v138, v138 op_sel:[0,1,0] op_sel_hi:[0,0,0]
	s_setprio 0
	s_barrier
	s_add_i32 s46, s46, 2
	s_addk_i32 s44, 0x100
	s_addk_i32 s45, 0x100
	s_cmp_gt_u32 s46, 13
	s_cbranch_scc0 .LBB0_1448
	s_branch .Lpeel_after_1448

;     __device__ __forceinline__ bool next(int i, Unit& u) const { u.aux = 0; return t.map(i, u.pm, u.pn); }
;     __device__ __forceinline__ bool next(int i, Unit& u) const { u.aux = i & 1; return t.map(i >> 1, u.pm, u.pn); }
; #define PG8_WAIT_V(n) asm volatile("s_waitcnt vmcnt(" #n ")" ::: "memory")
; #define PG8_BAR __builtin_amdgcn_s_barrier()
; template <class Epi, class Sched, bool ALIGN_EPI, bool F8 = false, int F8SC = F8_SCALES>
; __device__ __forceinline__ void gemm_phase(PG8_LAS unsigned char* lds, const __amdgpu_buffer_rsrc_t rsrc, const int lda, const int ldb, const int K, const Sched& S, const Epi& E) {
;     ...
;     Unit cur, nxt; int ui = 0;
;     if (!S.next(0, cur)) return;
;     f32x4 acc[2][2][4][2];
;     PG8_ZERO();
;     i32x8 At[4], B0[2], B1[2];
;     unsigned cA, cB; S.bases(cur, cA, cB); cA = __builtin_amdgcn_readfirstlane(cA); cB = __builtin_amdgcn_readfirstlane(cB);
;     PG8_STAGE(PG8_SB(0, 0), cB, voffB); PG8_STAGE(PG8_SB(0, 1), cB + hsB, voffB); PG8_STAGE(PG8_SA(0, 0), cA, voffA); PG8_STAGE(PG8_SA(0, 1), cA + hsA, voffA);
;     if (wr == 1) PG8_BAR;
;     PG8_WAIT_V(2); PG8_BAR;
;     PG8_STAGE(PG8_SB(1, 0), cB + kstep, voffB); PG8_STAGE(PG8_SA(1, 0), cA + kstep, voffA); PG8_STAGE(PG8_SB(1, 1), cB + hsB + kstep, voffB);
;     PG8_WAIT_V(6); PG8_BAR;
;     for (;;) {
;         const bool has_next = S.next(ui + 1, nxt);
;         unsigned nA = cA, nB = cB; if (has_next) { S.bases(nxt, nA, nB); nA = __builtin_amdgcn_readfirstlane(nA); nB = __builtin_amdgcn_readfirstlane(nB); }
; #pragma unroll 1
;         for (int t = 0; t < nt; t += 2) {
;             const bool last = (t == nt - 2);
;             const unsigned a1 = cA + (unsigned)(t + 1) * kstep;
;             const unsigned a2 = last ? nA : cA + (unsigned)(t + 2) * kstep, b2 = last ? nB : cB + (unsigned)(t + 2) * kstep;
;             const unsigned a3 = a2 + kstep, b3 = b2 + kstep;
;             PG8_LDB(B0, 0, 0); PG8_LDB(B1, 0, 1); PG8_SCHED; PG8_LDA(At, 0, 0); PG8_STAGE(PG8_SA(1, 1), a1 + hsA, voffA);
;             PG8_WAIT_V(8); PG8_WAIT_L(0); PG8_BAR; PG8_MMA(0, 0, At, B0); PG8_MMA(0, 1, At, B1); PG8_BAR; PG8_SCHED;
;             PG8_LDA(At, 0, 1); PG8_STAGE(PG8_SB(0, 0), b2, voffB); PG8_STAGE(PG8_SB(0, 1), b2 + hsB, voffB); PG8_STAGE(PG8_SA(0, 0), a2, voffA);
;             PG8_WAIT_V(8); PG8_WAIT_L(0); PG8_BAR; PG8_MMA(1, 0, At, B0); PG8_MMA(1, 1, At, B1); PG8_BAR; PG8_SCHED;
.LBB0_1650:
	s_add_i32 s55, s55, 0x60080
	s_addk_i32 s56, 0x100
	s_mov_b32 s57, -2
	s_waitcnt vmcnt(25)
	s_waitcnt vmcnt(23)
	s_waitcnt vmcnt(21)
	s_waitcnt vmcnt(19)
	s_waitcnt vmcnt(17)
	s_waitcnt vmcnt(15)
	s_waitcnt vmcnt(14)
	ds_read_b128 v[102:105], v155
	ds_read_b128 v[106:109], v155 offset:1024
	ds_read_b128 v[114:117], v155 offset:2048
	ds_read_b128 v[118:121], v155 offset:3072
	ds_read_b128 v[162:165], v156
	ds_read_b128 v[166:169], v156 offset:1024
	ds_read_b128 v[170:173], v156 offset:2048
	ds_read_b128 v[174:177], v156 offset:3072
	s_add_i32 s58, s55, 0xfffa0080
	s_cmp_eq_u32 s57, 12
	s_cselect_b32 s58, s5, s58
	s_cselect_b32 s60, s4, s56
	s_add_i32 s59, s58, 0x80
	s_add_i32 s61, s55, 0xfffe0000
	s_mov_b32 s80, s96
	s_mov_b32 m0, s65
	ds_read_b128 v[178:181], v157
	ds_read_b128 v[182:185], v157 offset:1024
	ds_read_b128 v[186:189], v157 offset:2048
	ds_read_b128 v[190:193], v157 offset:3072
	ds_read_b128 v[194:197], v157 offset:4096
	ds_read_b128 v[198:201], v157 offset:5120
	ds_read_b128 v[202:205], v157 offset:6144
	ds_read_b128 v[206:209], v157 offset:7168
	buffer_load_dwordx4 v1, s[80:83], s61 offen lds
	s_mov_b32 m0, s66
	s_nop 0
	buffer_load_dwordx4 v1, s[80:83], s55 offen lds
	s_waitcnt vmcnt(8)
	s_waitcnt lgkmcnt(0)
	s_barrier
	s_setprio 1
	s_waitcnt lgkmcnt(6)
	v_mfma_scale_f32_16x16x128_f8f6f4 v[142:145], v[102:109], v[178:185], 0, v158, v158 op_sel:[0,1,0] op_sel_hi:[0,0,0]
	v_mfma_scale_f32_16x16x128_f8f6f4 v[138:141], v[114:121], v[178:185], 0, v158, v158 op_sel:[0,1,0] op_sel_hi:[0,0,0]
	s_waitcnt lgkmcnt(4)
	v_mfma_scale_f32_16x16x128_f8f6f4 v[134:137], v[102:109], v[186:193], 0, v158, v158 op_sel:[0,1,0] op_sel_hi:[0,0,0]
	v_mfma_scale_f32_16x16x128_f8f6f4 v[110:113], v[114:121], v[186:193], 0, v158, v158 op_sel:[0,1,0] op_sel_hi:[0,0,0]
	s_waitcnt lgkmcnt(2)
	v_mfma_scale_f32_16x16x128_f8f6f4 v[148:151], v[102:109], v[194:201], 0, v158, v158 op_sel:[0,1,0] op_sel_hi:[0,0,0]
	v_mfma_scale_f32_16x16x128_f8f6f4 v[210:213], v[114:121], v[194:201], 0, v158, v158 op_sel:[0,1,0] op_sel_hi:[0,0,0]
	s_waitcnt lgkmcnt(0)
	v_mfma_scale_f32_16x16x128_f8f6f4 v[214:217], v[102:109], v[202:209], 0, v158, v158 op_sel:[0,1,0] op_sel_hi:[0,0,0]
	v_mfma_scale_f32_16x16x128_f8f6f4 v[218:221], v[114:121], v[202:209], 0, v158, v158 op_sel:[0,1,0] op_sel_hi:[0,0,0]
	s_setprio 0
	s_setprio 1
	v_mfma_scale_f32_16x16x128_f8f6f4 v[130:133], v[162:169], v[178:185], 0, v158, v158 op_sel:[0,1,0] op_sel_hi:[0,0,0]
	v_mfma_scale_f32_16x16x128_f8f6f4 v[126:129], v[170:177], v[178:185], 0, v158, v158 op_sel:[0,1,0] op_sel_hi:[0,0,0]
	v_mfma_scale_f32_16x16x128_f8f6f4 v[122:125], v[162:169], v[186:193], 0, v158, v158 op_sel:[0,1,0] op_sel_hi:[0,0,0]
	v_mfma_scale_f32_16x16x128_f8f6f4 v[98:101], v[170:177], v[186:193], 0, v158, v158 op_sel:[0,1,0] op_sel_hi:[0,0,0]
	v_mfma_scale_f32_16x16x128_f8f6f4 v[178:181], v[162:169], v[194:201], 0, v158, v158 op_sel:[0,1,0] op_sel_hi:[0,0,0]
	v_mfma_scale_f32_16x16x128_f8f6f4 v[182:185], v[170:177], v[194:201], 0, v158, v158 op_sel:[0,1,0] op_sel_hi:[0,0,0]
	v_mfma_scale_f32_16x16x128_f8f6f4 v[186:189], v[162:169], v[202:209], 0, v158, v158 op_sel:[0,1,0] op_sel_hi:[0,0,0]
	v_mfma_scale_f32_16x16x128_f8f6f4 v[190:193], v[170:177], v[202:209], 0, v158, v158 op_sel:[0,1,0] op_sel_hi:[0,0,0]
	s_setprio 0
	s_barrier
	s_mov_b32 m0, s28
	s_nop 3
	ds_read_b128 v[66:69], v157 offset:16384
	ds_read_b128 v[70:73], v157 offset:17408
	ds_read_b128 v[74:77], v157 offset:18432
	ds_read_b128 v[78:81], v157 offset:19456
	ds_read_b128 v[82:85], v157 offset:20480
	ds_read_b128 v[86:89], v157 offset:21504
	ds_read_b128 v[90:93], v157 offset:22528
	ds_read_b128 v[94:97], v157 offset:23552
	buffer_load_dwordx4 v154, s[80:83], s60 offen lds
	s_add_i32 s61, s60, 0x20000
	s_mov_b32 m0, s29
	s_nop 0
	buffer_load_dwordx4 v154, s[80:83], s61 offen lds
	s_add_i32 s61, s60, 0x40000
	s_mov_b32 m0, s30
	s_nop 0
	buffer_load_dwordx4 v154, s[80:83], s61 offen lds
	s_add_i32 s61, s60, 0x60000
	s_mov_b32 m0, s31
	s_nop 0
	buffer_load_dwordx4 v154, s[80:83], s61 offen lds
	s_mov_b32 m0, s27
	s_add_i32 s61, s58, 0x20000
	buffer_load_dwordx4 v1, s[80:83], s58 offen lds
	s_mov_b32 m0, s33
	s_nop 0
	buffer_load_dwordx4 v1, s[80:83], s61 offen lds
	s_waitcnt vmcnt(8)
	s_waitcnt lgkmcnt(0)
	s_barrier
	s_setprio 1
	s_waitcnt lgkmcnt(6)
	v_mfma_scale_f32_16x16x128_f8f6f4 v[62:65], v[102:109], v[66:73], 0, v158, v158 op_sel:[0,1,0] op_sel_hi:[0,0,0]
	v_mfma_scale_f32_16x16x128_f8f6f4 v[54:57], v[114:121], v[66:73], 0, v158, v158 op_sel:[0,1,0] op_sel_hi:[0,0,0]
	s_waitcnt lgkmcnt(4)
	v_mfma_scale_f32_16x16x128_f8f6f4 v[46:49], v[102:109], v[74:81], 0, v158, v158 op_sel:[0,1,0] op_sel_hi:[0,0,0]
	v_mfma_scale_f32_16x16x128_f8f6f4 v[202:205], v[114:121], v[74:81], 0, v158, v158 op_sel:[0,1,0] op_sel_hi:[0,0,0]
	s_waitcnt lgkmcnt(2)
	v_mfma_scale_f32_16x16x128_f8f6f4 v[206:209], v[102:109], v[82:89], 0, v158, v158 op_sel:[0,1,0] op_sel_hi:[0,0,0]
	v_mfma_scale_f32_16x16x128_f8f6f4 v[222:225], v[114:121], v[82:89], 0, v158, v158 op_sel:[0,1,0] op_sel_hi:[0,0,0]
	s_waitcnt lgkmcnt(0)
	v_mfma_scale_f32_16x16x128_f8f6f4 v[226:229], v[102:109], v[90:97], 0, v158, v158 op_sel:[0,1,0] op_sel_hi:[0,0,0]
	v_mfma_scale_f32_16x16x128_f8f6f4 v[230:233], v[114:121], v[90:97], 0, v158, v158 op_sel:[0,1,0] op_sel_hi:[0,0,0]
	s_setprio 0
	s_setprio 1
	v_mfma_scale_f32_16x16x128_f8f6f4 v[58:61], v[162:169], v[66:73], 0, v158, v158 op_sel:[0,1,0] op_sel_hi:[0,0,0]
	v_mfma_scale_f32_16x16x128_f8f6f4 v[50:53], v[170:177], v[66:73], 0, v158, v158 op_sel:[0,1,0] op_sel_hi:[0,0,0]
	v_mfma_scale_f32_16x16x128_f8f6f4 v[42:45], v[162:169], v[74:81], 0, v158, v158 op_sel:[0,1,0] op_sel_hi:[0,0,0]
	v_mfma_scale_f32_16x16x128_f8f6f4 v[234:237], v[170:177], v[74:81], 0, v158, v158 op_sel:[0,1,0] op_sel_hi:[0,0,0]
	v_mfma_scale_f32_16x16x128_f8f6f4 v[238:241], v[162:169], v[82:89], 0, v158, v158 op_sel:[0,1,0] op_sel_hi:[0,0,0]
	v_mfma_scale_f32_16x16x128_f8f6f4 v[242:245], v[170:177], v[82:89], 0, v158, v158 op_sel:[0,1,0] op_sel_hi:[0,0,0]
	v_mfma_scale_f32_16x16x128_f8f6f4 v[246:249], v[162:169], v[90:97], 0, v158, v158 op_sel:[0,1,0] op_sel_hi:[0,0,0]
	v_mfma_scale_f32_16x16x128_f8f6f4 v[250:253], v[170:177], v[90:97], 0, v158, v158 op_sel:[0,1,0] op_sel_hi:[0,0,0]
	s_setprio 0
	s_barrier
; #define PG8_STAGE(bufoff, goff, voff) do { _Pragma("unroll") for (int _i = 0; _i < 2; ++_i) \
;         __builtin_amdgcn_raw_ptr_buffer_load_lds(rsrc, (PG8_LAS void*)(lds + (bufoff) + ldsw + _i * 8192), 16, (int)(voff), (int)((goff) + _i * p1##voff), 0, 0); } while (0)
; #define PG8_LDA(dst, b, h) do { _Pragma("unroll") for (int m = 0; m < 4; ++m) dst[m] = PG8_LD8(lds + PG8_SA(b, h) + aoff + m * 2048); } while (0)
; #define PG8_LDB(dst, b, h) do { _Pragma("unroll") for (int n = 0; n < 2; ++n) dst[n] = PG8_LD8(lds + PG8_SB(b, h) + boff + n * 2048); } while (0)
; #define PG8_WAIT_V(n) asm volatile("s_waitcnt vmcnt(" #n ")" ::: "memory")
; #define PG8_WAIT_L(n) asm volatile("s_waitcnt lgkmcnt(" #n ")" ::: "memory")
; #define PG8_BAR __builtin_amdgcn_s_barrier()
; #define PG8_SCHED __builtin_amdgcn_sched_barrier(0)
; template <class Epi, class Sched, bool ALIGN_EPI, bool F8 = false, int F8SC = F8_SCALES>
; __device__ __forceinline__ void gemm_phase(PG8_LAS unsigned char* lds, const __amdgpu_buffer_rsrc_t rsrc, const int lda, const int ldb, const int K, const Sched& S, const Epi& E) {
;     ...
;             PG8_LDB(B0, 1, 0); PG8_LDB(B1, 1, 1); PG8_SCHED; PG8_LDA(At, 1, 0); PG8_STAGE(PG8_SA(0, 1), a2 + hsA, voffA);
;             PG8_WAIT_V(8); PG8_WAIT_L(0); PG8_BAR; PG8_MMA(0, 0, At, B0); PG8_MMA(0, 1, At, B1); PG8_BAR; PG8_SCHED;
;             PG8_LDA(At, 1, 1); PG8_STAGE(PG8_SB(1, 0), b3, voffB); PG8_STAGE(PG8_SB(1, 1), b3 + hsB, voffB); PG8_STAGE(PG8_SA(1, 0), a3, voffA);
;             PG8_WAIT_V(8); PG8_WAIT_L(0); PG8_BAR; PG8_MMA(1, 0, At, B0); PG8_MMA(1, 1, At, B1); PG8_BAR; PG8_SCHED;
;         }
	s_nop 4
	ds_read_b128 v[2:5], v159
	ds_read_b128 v[6:9], v159 offset:1024
	ds_read_b128 v[102:105], v159 offset:2048
	ds_read_b128 v[106:109], v159 offset:3072
	ds_read_b128 v[114:117], v160
	ds_read_b128 v[118:121], v160 offset:1024
	ds_read_b128 v[162:165], v160 offset:2048
	ds_read_b128 v[166:169], v160 offset:3072
	s_mov_b32 m0, s34
	s_add_i32 s61, s58, 0x40000
	ds_read_b128 v[10:13], v157 offset:32768
	ds_read_b128 v[14:17], v157 offset:33792
	ds_read_b128 v[18:21], v157 offset:34816
	ds_read_b128 v[22:25], v157 offset:35840
	ds_read_b128 v[26:29], v157 offset:36864
	ds_read_b128 v[30:33], v157 offset:37888
	ds_read_b128 v[34:37], v157 offset:38912
	ds_read_b128 v[38:41], v157 offset:39936
	buffer_load_dwordx4 v1, s[80:83], s61 offen lds
	s_add_i32 s61, s58, 0x60000
	s_mov_b32 m0, s35
	s_nop 0
	buffer_load_dwordx4 v1, s[80:83], s61 offen lds
	s_waitcnt vmcnt(8)
	s_waitcnt lgkmcnt(0)
	s_barrier
	s_setprio 1
	s_waitcnt lgkmcnt(6)
	v_mfma_scale_f32_16x16x128_f8f6f4 v[142:145], v[2:9], v[10:17], v[142:145], v158, v158 op_sel:[0,1,0] op_sel_hi:[0,0,0]
	v_mfma_scale_f32_16x16x128_f8f6f4 v[138:141], v[102:109], v[10:17], v[138:141], v158, v158 op_sel:[0,1,0] op_sel_hi:[0,0,0]
	s_waitcnt lgkmcnt(4)
	v_mfma_scale_f32_16x16x128_f8f6f4 v[134:137], v[2:9], v[18:25], v[134:137], v158, v158 op_sel:[0,1,0] op_sel_hi:[0,0,0]
	v_mfma_scale_f32_16x16x128_f8f6f4 v[110:113], v[102:109], v[18:25], v[110:113], v158, v158 op_sel:[0,1,0] op_sel_hi:[0,0,0]
	s_waitcnt lgkmcnt(2)
	v_mfma_scale_f32_16x16x128_f8f6f4 v[94:97], v[2:9], v[26:33], v[148:151], v158, v158 op_sel:[0,1,0] op_sel_hi:[0,0,0]
	v_mfma_scale_f32_16x16x128_f8f6f4 v[86:89], v[102:109], v[26:33], v[210:213], v158, v158 op_sel:[0,1,0] op_sel_hi:[0,0,0]
	s_waitcnt lgkmcnt(0)
	v_mfma_scale_f32_16x16x128_f8f6f4 v[78:81], v[2:9], v[34:41], v[214:217], v158, v158 op_sel:[0,1,0] op_sel_hi:[0,0,0]
	v_mfma_scale_f32_16x16x128_f8f6f4 v[70:73], v[102:109], v[34:41], v[218:221], v158, v158 op_sel:[0,1,0] op_sel_hi:[0,0,0]
	s_setprio 0
	s_setprio 1
	v_mfma_scale_f32_16x16x128_f8f6f4 v[130:133], v[114:121], v[10:17], v[130:133], v158, v158 op_sel:[0,1,0] op_sel_hi:[0,0,0]
	v_mfma_scale_f32_16x16x128_f8f6f4 v[126:129], v[162:169], v[10:17], v[126:129], v158, v158 op_sel:[0,1,0] op_sel_hi:[0,0,0]
	v_mfma_scale_f32_16x16x128_f8f6f4 v[122:125], v[114:121], v[18:25], v[122:125], v158, v158 op_sel:[0,1,0] op_sel_hi:[0,0,0]
	v_mfma_scale_f32_16x16x128_f8f6f4 v[98:101], v[162:169], v[18:25], v[98:101], v158, v158 op_sel:[0,1,0] op_sel_hi:[0,0,0]
	v_mfma_scale_f32_16x16x128_f8f6f4 v[90:93], v[114:121], v[26:33], v[178:181], v158, v158 op_sel:[0,1,0] op_sel_hi:[0,0,0]
	v_mfma_scale_f32_16x16x128_f8f6f4 v[82:85], v[162:169], v[26:33], v[182:185], v158, v158 op_sel:[0,1,0] op_sel_hi:[0,0,0]
	v_mfma_scale_f32_16x16x128_f8f6f4 v[74:77], v[114:121], v[34:41], v[186:189], v158, v158 op_sel:[0,1,0] op_sel_hi:[0,0,0]
	v_mfma_scale_f32_16x16x128_f8f6f4 v[66:69], v[162:169], v[34:41], v[190:193], v158, v158 op_sel:[0,1,0] op_sel_hi:[0,0,0]
	s_setprio 0
	s_barrier
	s_mov_b32 m0, s39
	s_add_i32 s61, s60, 0x80
	ds_read_b128 v[170:173], v157 offset:49152
	ds_read_b128 v[174:177], v157 offset:50176
	ds_read_b128 v[178:181], v157 offset:51200
	ds_read_b128 v[182:185], v157 offset:52224
	ds_read_b128 v[186:189], v157 offset:53248
	ds_read_b128 v[190:193], v157 offset:54272
	ds_read_b128 v[194:197], v157 offset:55296
	ds_read_b128 v[198:201], v157 offset:56320
	buffer_load_dwordx4 v154, s[80:83], s61 offen lds
	s_add_i32 s61, s60, 0x20080
	s_mov_b32 m0, s40
	s_add_i32 s58, s58, 0x20080
	buffer_load_dwordx4 v154, s[80:83], s61 offen lds
	s_add_i32 s61, s60, 0x40080
	s_mov_b32 m0, s43
	s_add_i32 s60, s60, 0x60080
	buffer_load_dwordx4 v154, s[80:83], s61 offen lds
	s_mov_b32 m0, s64
	s_nop 0
	buffer_load_dwordx4 v154, s[80:83], s60 offen lds
	s_mov_b32 m0, s41
	s_nop 0
	buffer_load_dwordx4 v1, s[80:83], s59 offen lds
	s_mov_b32 m0, s42
	s_nop 0
	buffer_load_dwordx4 v1, s[80:83], s58 offen lds
	s_waitcnt vmcnt(8)
	s_waitcnt lgkmcnt(0)
	s_barrier
	s_setprio 1
	s_waitcnt lgkmcnt(6)
	v_mfma_scale_f32_16x16x128_f8f6f4 v[62:65], v[2:9], v[170:177], v[62:65], v158, v158 op_sel:[0,1,0] op_sel_hi:[0,0,0]
	v_mfma_scale_f32_16x16x128_f8f6f4 v[54:57], v[102:109], v[170:177], v[54:57], v158, v158 op_sel:[0,1,0] op_sel_hi:[0,0,0]
	s_waitcnt lgkmcnt(4)
	v_mfma_scale_f32_16x16x128_f8f6f4 v[46:49], v[2:9], v[178:185], v[46:49], v158, v158 op_sel:[0,1,0] op_sel_hi:[0,0,0]
	v_mfma_scale_f32_16x16x128_f8f6f4 v[38:41], v[102:109], v[178:185], v[202:205], v158, v158 op_sel:[0,1,0] op_sel_hi:[0,0,0]
	s_waitcnt lgkmcnt(2)
	v_mfma_scale_f32_16x16x128_f8f6f4 v[30:33], v[2:9], v[186:193], v[206:209], v158, v158 op_sel:[0,1,0] op_sel_hi:[0,0,0]
	v_mfma_scale_f32_16x16x128_f8f6f4 v[22:25], v[102:109], v[186:193], v[222:225], v158, v158 op_sel:[0,1,0] op_sel_hi:[0,0,0]
	s_waitcnt lgkmcnt(0)
	v_mfma_scale_f32_16x16x128_f8f6f4 v[14:17], v[2:9], v[194:201], v[226:229], v158, v158 op_sel:[0,1,0] op_sel_hi:[0,0,0]
	v_mfma_scale_f32_16x16x128_f8f6f4 v[6:9], v[102:109], v[194:201], v[230:233], v158, v158 op_sel:[0,1,0] op_sel_hi:[0,0,0]
	s_setprio 0
	s_setprio 1
	v_mfma_scale_f32_16x16x128_f8f6f4 v[58:61], v[114:121], v[170:177], v[58:61], v158, v158 op_sel:[0,1,0] op_sel_hi:[0,0,0]
	v_mfma_scale_f32_16x16x128_f8f6f4 v[50:53], v[162:169], v[170:177], v[50:53], v158, v158 op_sel:[0,1,0] op_sel_hi:[0,0,0]
	v_mfma_scale_f32_16x16x128_f8f6f4 v[42:45], v[114:121], v[178:185], v[42:45], v158, v158 op_sel:[0,1,0] op_sel_hi:[0,0,0]
	v_mfma_scale_f32_16x16x128_f8f6f4 v[34:37], v[162:169], v[178:185], v[234:237], v158, v158 op_sel:[0,1,0] op_sel_hi:[0,0,0]
	v_mfma_scale_f32_16x16x128_f8f6f4 v[26:29], v[114:121], v[186:193], v[238:241], v158, v158 op_sel:[0,1,0] op_sel_hi:[0,0,0]
	v_mfma_scale_f32_16x16x128_f8f6f4 v[18:21], v[162:169], v[186:193], v[242:245], v158, v158 op_sel:[0,1,0] op_sel_hi:[0,0,0]
	v_mfma_scale_f32_16x16x128_f8f6f4 v[10:13], v[114:121], v[194:201], v[246:249], v158, v158 op_sel:[0,1,0] op_sel_hi:[0,0,0]
	v_mfma_scale_f32_16x16x128_f8f6f4 v[2:5], v[162:169], v[194:201], v[250:253], v158, v158 op_sel:[0,1,0] op_sel_hi:[0,0,0]
	s_setprio 0
	s_barrier
	s_add_i32 s57, s57, 2
	s_addk_i32 s55, 0x100
	s_addk_i32 s56, 0x100
	s_cmp_gt_u32 s57, 13
	s_cbranch_scc0 .LBB0_1651
	s_branch .Lpeel_after_1651

; #define PG8_BAR __builtin_amdgcn_s_barrier()
; template <class Epi, class Sched, bool ALIGN_EPI, bool F8 = false, int F8SC = F8_SCALES>
; __device__ __forceinline__ void gemm_phase(PG8_LAS unsigned char* lds, const __amdgpu_buffer_rsrc_t rsrc, const int lda, const int ldb, const int K, const Sched& S, const Epi& E) {
;     ...
;         if constexpr (ALIGN_EPI) { if (wr == 0) PG8_BAR; }
.Lpeel_after_1651:
	s_and_b64 vcc, exec, s[8:9]
	s_cbranch_vccz .LBB0_1654
	s_barrier

; #define PG8_STAGE(bufoff, goff, voff) do { _Pragma("unroll") for (int _i = 0; _i < 2; ++_i) \
;         __builtin_amdgcn_raw_ptr_buffer_load_lds(rsrc, (PG8_LAS void*)(lds + (bufoff) + ldsw + _i * 8192), 16, (int)(voff), (int)((goff) + _i * p1##voff), 0, 0); } while (0)
; #define PG8_LDA(dst, b, h) do { _Pragma("unroll") for (int m = 0; m < 4; ++m) dst[m] = PG8_LD8(lds + PG8_SA(b, h) + aoff + m * 2048); } while (0)
; #define PG8_LDB(dst, b, h) do { _Pragma("unroll") for (int n = 0; n < 2; ++n) dst[n] = PG8_LD8(lds + PG8_SB(b, h) + boff + n * 2048); } while (0)
; #define PG8_WAIT_V(n) asm volatile("s_waitcnt vmcnt(" #n ")" ::: "memory")
; #define PG8_WAIT_L(n) asm volatile("s_waitcnt lgkmcnt(" #n ")" ::: "memory")
; #define PG8_BAR __builtin_amdgcn_s_barrier()
; #define PG8_SCHED __builtin_amdgcn_sched_barrier(0)
; template <class Epi, class Sched, bool ALIGN_EPI, bool F8 = false, int F8SC = F8_SCALES>
; __device__ __forceinline__ void gemm_phase(PG8_LAS unsigned char* lds, const __amdgpu_buffer_rsrc_t rsrc, const int lda, const int ldb, const int K, const Sched& S, const Epi& E) {
;     ...
;         for (int t = 0; t < nt; t += 2) {
;             const bool last = (t == nt - 2);
;             const unsigned a1 = cA + (unsigned)(t + 1) * kstep;
;             const unsigned a2 = last ? nA : cA + (unsigned)(t + 2) * kstep, b2 = last ? nB : cB + (unsigned)(t + 2) * kstep;
;             const unsigned a3 = a2 + kstep, b3 = b2 + kstep;
;             PG8_LDB(B0, 0, 0); PG8_LDB(B1, 0, 1); PG8_SCHED; PG8_LDA(At, 0, 0); PG8_STAGE(PG8_SA(1, 1), a1 + hsA, voffA);
;             PG8_WAIT_V(8); PG8_WAIT_L(0); PG8_BAR; PG8_MMA(0, 0, At, B0); PG8_MMA(0, 1, At, B1); PG8_BAR; PG8_SCHED;
;             PG8_LDA(At, 0, 1); PG8_STAGE(PG8_SB(0, 0), b2, voffB); PG8_STAGE(PG8_SB(0, 1), b2 + hsB, voffB); PG8_STAGE(PG8_SA(0, 0), a2, voffA);
;             PG8_WAIT_V(8); PG8_WAIT_L(0); PG8_BAR; PG8_MMA(1, 0, At, B0); PG8_MMA(1, 1, At, B1); PG8_BAR; PG8_SCHED;
.LBB0_1724:
	s_add_i32 s4, s50, 0x60080
	s_add_i32 s5, s49, 0x100
	s_mov_b32 s49, -2
	s_waitcnt vmcnt(25)
	s_waitcnt vmcnt(24)
	s_waitcnt vmcnt(21)
	s_waitcnt vmcnt(20)
	s_waitcnt vmcnt(17)
	s_waitcnt vmcnt(16)
	s_waitcnt vmcnt(15)
	s_waitcnt vmcnt(14)
	ds_read_b128 v[130:133], v169
	ds_read_b128 v[134:137], v169 offset:1024
	ds_read_b128 v[138:141], v169 offset:2048
	ds_read_b128 v[142:145], v169 offset:3072
	ds_read_b128 v[150:153], v170
	ds_read_b128 v[154:157], v170 offset:1024
	ds_read_b128 v[158:161], v170 offset:2048
	ds_read_b128 v[162:165], v170 offset:3072
	s_add_i32 s50, s4, 0xfffa0080
	s_cmp_eq_u32 s49, 12
	s_cselect_b32 s50, s47, s50
	s_cselect_b32 s52, s46, s5
	s_add_i32 s51, s50, 0x80
	s_add_i32 s53, s4, 0xfffe0000
	s_mov_b32 s80, s96
	s_mov_b32 m0, s30
	ds_read_b128 v[176:179], v171
	ds_read_b128 v[180:183], v171 offset:1024
	ds_read_b128 v[184:187], v171 offset:2048
	ds_read_b128 v[188:191], v171 offset:3072
	ds_read_b128 v[192:195], v171 offset:4096
	ds_read_b128 v[196:199], v171 offset:5120
	ds_read_b128 v[200:203], v171 offset:6144
	ds_read_b128 v[204:207], v171 offset:7168
	buffer_load_dwordx4 v1, s[80:83], s53 offen lds
	s_mov_b32 m0, s31
	s_nop 0
	buffer_load_dwordx4 v1, s[80:83], s4 offen lds
	s_waitcnt vmcnt(8)
	s_waitcnt lgkmcnt(0)
	s_barrier
	s_setprio 1
	s_waitcnt lgkmcnt(6)
	v_mfma_scale_f32_16x16x128_f8f6f4 v[126:129], v[130:137], v[176:183], 0, v172, v172 op_sel:[0,1,0] op_sel_hi:[0,0,0]
	v_mfma_scale_f32_16x16x128_f8f6f4 v[122:125], v[138:145], v[176:183], 0, v172, v172 op_sel:[0,1,0] op_sel_hi:[0,0,0]
	s_waitcnt lgkmcnt(4)
	v_mfma_scale_f32_16x16x128_f8f6f4 v[110:113], v[130:137], v[184:191], 0, v172, v172 op_sel:[0,1,0] op_sel_hi:[0,0,0]
	v_mfma_scale_f32_16x16x128_f8f6f4 v[106:109], v[138:145], v[184:191], 0, v172, v172 op_sel:[0,1,0] op_sel_hi:[0,0,0]
	s_waitcnt lgkmcnt(2)
	v_mfma_scale_f32_16x16x128_f8f6f4 v[208:211], v[130:137], v[192:199], 0, v172, v172 op_sel:[0,1,0] op_sel_hi:[0,0,0]
	v_mfma_scale_f32_16x16x128_f8f6f4 v[212:215], v[138:145], v[192:199], 0, v172, v172 op_sel:[0,1,0] op_sel_hi:[0,0,0]
	s_waitcnt lgkmcnt(0)
	v_mfma_scale_f32_16x16x128_f8f6f4 v[216:219], v[130:137], v[200:207], 0, v172, v172 op_sel:[0,1,0] op_sel_hi:[0,0,0]
	v_mfma_scale_f32_16x16x128_f8f6f4 v[220:223], v[138:145], v[200:207], 0, v172, v172 op_sel:[0,1,0] op_sel_hi:[0,0,0]
	s_setprio 0
	s_setprio 1
	v_mfma_scale_f32_16x16x128_f8f6f4 v[118:121], v[150:157], v[176:183], 0, v172, v172 op_sel:[0,1,0] op_sel_hi:[0,0,0]
	v_mfma_scale_f32_16x16x128_f8f6f4 v[114:117], v[158:165], v[176:183], 0, v172, v172 op_sel:[0,1,0] op_sel_hi:[0,0,0]
	v_mfma_scale_f32_16x16x128_f8f6f4 v[102:105], v[150:157], v[184:191], 0, v172, v172 op_sel:[0,1,0] op_sel_hi:[0,0,0]
	v_mfma_scale_f32_16x16x128_f8f6f4 v[98:101], v[158:165], v[184:191], 0, v172, v172 op_sel:[0,1,0] op_sel_hi:[0,0,0]
	v_mfma_scale_f32_16x16x128_f8f6f4 v[176:179], v[150:157], v[192:199], 0, v172, v172 op_sel:[0,1,0] op_sel_hi:[0,0,0]
	v_mfma_scale_f32_16x16x128_f8f6f4 v[180:183], v[158:165], v[192:199], 0, v172, v172 op_sel:[0,1,0] op_sel_hi:[0,0,0]
	v_mfma_scale_f32_16x16x128_f8f6f4 v[184:187], v[150:157], v[200:207], 0, v172, v172 op_sel:[0,1,0] op_sel_hi:[0,0,0]
	v_mfma_scale_f32_16x16x128_f8f6f4 v[188:191], v[158:165], v[200:207], 0, v172, v172 op_sel:[0,1,0] op_sel_hi:[0,0,0]
	s_setprio 0
	s_barrier
	s_mov_b32 m0, s16
	s_nop 3
	ds_read_b128 v[66:69], v171 offset:16384
	ds_read_b128 v[70:73], v171 offset:17408
	ds_read_b128 v[74:77], v171 offset:18432
	ds_read_b128 v[78:81], v171 offset:19456
	ds_read_b128 v[82:85], v171 offset:20480
	ds_read_b128 v[86:89], v171 offset:21504
	ds_read_b128 v[90:93], v171 offset:22528
	ds_read_b128 v[94:97], v171 offset:23552
	buffer_load_dwordx4 v168, s[80:83], s52 offen lds
	s_add_i32 s53, s52, 0x20000
	s_mov_b32 m0, s17
	s_nop 0
	buffer_load_dwordx4 v168, s[80:83], s53 offen lds
	s_add_i32 s53, s52, 0x40000
	s_mov_b32 m0, s18
	s_nop 0
	buffer_load_dwordx4 v168, s[80:83], s53 offen lds
	s_add_i32 s53, s52, 0x60000
	s_mov_b32 m0, s19
	s_nop 0
	buffer_load_dwordx4 v168, s[80:83], s53 offen lds
	s_mov_b32 m0, s15
	s_add_i32 s53, s50, 0x20000
	buffer_load_dwordx4 v1, s[80:83], s50 offen lds
	s_mov_b32 m0, s20
	s_nop 0
	buffer_load_dwordx4 v1, s[80:83], s53 offen lds
	s_waitcnt vmcnt(8)
	s_waitcnt lgkmcnt(0)
	s_barrier
	s_setprio 1
	s_waitcnt lgkmcnt(6)
	v_mfma_scale_f32_16x16x128_f8f6f4 v[62:65], v[130:137], v[66:73], 0, v172, v172 op_sel:[0,1,0] op_sel_hi:[0,0,0]
	v_mfma_scale_f32_16x16x128_f8f6f4 v[58:61], v[138:145], v[66:73], 0, v172, v172 op_sel:[0,1,0] op_sel_hi:[0,0,0]
	s_waitcnt lgkmcnt(4)
	v_mfma_scale_f32_16x16x128_f8f6f4 v[192:195], v[130:137], v[74:81], 0, v172, v172 op_sel:[0,1,0] op_sel_hi:[0,0,0]
	v_mfma_scale_f32_16x16x128_f8f6f4 v[196:199], v[138:145], v[74:81], 0, v172, v172 op_sel:[0,1,0] op_sel_hi:[0,0,0]
	s_waitcnt lgkmcnt(2)
	v_mfma_scale_f32_16x16x128_f8f6f4 v[200:203], v[130:137], v[82:89], 0, v172, v172 op_sel:[0,1,0] op_sel_hi:[0,0,0]
	v_mfma_scale_f32_16x16x128_f8f6f4 v[204:207], v[138:145], v[82:89], 0, v172, v172 op_sel:[0,1,0] op_sel_hi:[0,0,0]
	s_waitcnt lgkmcnt(0)
	v_mfma_scale_f32_16x16x128_f8f6f4 v[224:227], v[130:137], v[90:97], 0, v172, v172 op_sel:[0,1,0] op_sel_hi:[0,0,0]
	v_mfma_scale_f32_16x16x128_f8f6f4 v[228:231], v[138:145], v[90:97], 0, v172, v172 op_sel:[0,1,0] op_sel_hi:[0,0,0]
	s_setprio 0
	s_setprio 1
	v_mfma_scale_f32_16x16x128_f8f6f4 v[54:57], v[150:157], v[66:73], 0, v172, v172 op_sel:[0,1,0] op_sel_hi:[0,0,0]
	v_mfma_scale_f32_16x16x128_f8f6f4 v[50:53], v[158:165], v[66:73], 0, v172, v172 op_sel:[0,1,0] op_sel_hi:[0,0,0]
	v_mfma_scale_f32_16x16x128_f8f6f4 v[232:235], v[150:157], v[74:81], 0, v172, v172 op_sel:[0,1,0] op_sel_hi:[0,0,0]
	v_mfma_scale_f32_16x16x128_f8f6f4 v[236:239], v[158:165], v[74:81], 0, v172, v172 op_sel:[0,1,0] op_sel_hi:[0,0,0]
	v_mfma_scale_f32_16x16x128_f8f6f4 v[240:243], v[150:157], v[82:89], 0, v172, v172 op_sel:[0,1,0] op_sel_hi:[0,0,0]
	v_mfma_scale_f32_16x16x128_f8f6f4 v[244:247], v[158:165], v[82:89], 0, v172, v172 op_sel:[0,1,0] op_sel_hi:[0,0,0]
	v_mfma_scale_f32_16x16x128_f8f6f4 v[248:251], v[150:157], v[90:97], 0, v172, v172 op_sel:[0,1,0] op_sel_hi:[0,0,0]
	v_mfma_scale_f32_16x16x128_f8f6f4 v[146:149], v[158:165], v[90:97], 0, v172, v172 op_sel:[0,1,0] op_sel_hi:[0,0,0]
	s_setprio 0
	s_barrier
; #define PG8_STAGE(bufoff, goff, voff) do { _Pragma("unroll") for (int _i = 0; _i < 2; ++_i) \
;         __builtin_amdgcn_raw_ptr_buffer_load_lds(rsrc, (PG8_LAS void*)(lds + (bufoff) + ldsw + _i * 8192), 16, (int)(voff), (int)((goff) + _i * p1##voff), 0, 0); } while (0)
; #define PG8_LDA(dst, b, h) do { _Pragma("unroll") for (int m = 0; m < 4; ++m) dst[m] = PG8_LD8(lds + PG8_SA(b, h) + aoff + m * 2048); } while (0)
; #define PG8_LDB(dst, b, h) do { _Pragma("unroll") for (int n = 0; n < 2; ++n) dst[n] = PG8_LD8(lds + PG8_SB(b, h) + boff + n * 2048); } while (0)
; #define PG8_WAIT_V(n) asm volatile("s_waitcnt vmcnt(" #n ")" ::: "memory")
; #define PG8_WAIT_L(n) asm volatile("s_waitcnt lgkmcnt(" #n ")" ::: "memory")
; #define PG8_BAR __builtin_amdgcn_s_barrier()
; #define PG8_SCHED __builtin_amdgcn_sched_barrier(0)
; template <class Epi, class Sched, bool ALIGN_EPI, bool F8 = false, int F8SC = F8_SCALES>
; __device__ __forceinline__ void gemm_phase(PG8_LAS unsigned char* lds, const __amdgpu_buffer_rsrc_t rsrc, const int lda, const int ldb, const int K, const Sched& S, const Epi& E) {
;     ...
;             PG8_LDB(B0, 1, 0); PG8_LDB(B1, 1, 1); PG8_SCHED; PG8_LDA(At, 1, 0); PG8_STAGE(PG8_SA(0, 1), a2 + hsA, voffA);
;             PG8_WAIT_V(8); PG8_WAIT_L(0); PG8_BAR; PG8_MMA(0, 0, At, B0); PG8_MMA(0, 1, At, B1); PG8_BAR; PG8_SCHED;
;             PG8_LDA(At, 1, 1); PG8_STAGE(PG8_SB(1, 0), b3, voffB); PG8_STAGE(PG8_SB(1, 1), b3 + hsB, voffB); PG8_STAGE(PG8_SA(1, 0), a3, voffA);
;             PG8_WAIT_V(8); PG8_WAIT_L(0); PG8_BAR; PG8_MMA(1, 0, At, B0); PG8_MMA(1, 1, At, B1); PG8_BAR; PG8_SCHED;
;         }
	s_nop 4
	ds_read_b128 v[2:5], v173
	ds_read_b128 v[6:9], v173 offset:1024
	ds_read_b128 v[18:21], v173 offset:2048
	ds_read_b128 v[22:25], v173 offset:3072
	ds_read_b128 v[130:133], v174
	ds_read_b128 v[134:137], v174 offset:1024
	ds_read_b128 v[138:141], v174 offset:2048
	ds_read_b128 v[142:145], v174 offset:3072
	s_mov_b32 m0, s21
	s_add_i32 s53, s50, 0x40000
	ds_read_b128 v[10:13], v171 offset:32768
	ds_read_b128 v[14:17], v171 offset:33792
	ds_read_b128 v[26:29], v171 offset:34816
	ds_read_b128 v[30:33], v171 offset:35840
	ds_read_b128 v[34:37], v171 offset:36864
	ds_read_b128 v[38:41], v171 offset:37888
	ds_read_b128 v[42:45], v171 offset:38912
	ds_read_b128 v[46:49], v171 offset:39936
	buffer_load_dwordx4 v1, s[80:83], s53 offen lds
	s_add_i32 s53, s50, 0x60000
	s_mov_b32 m0, s22
	s_nop 0
	buffer_load_dwordx4 v1, s[80:83], s53 offen lds
	s_waitcnt vmcnt(8)
	s_waitcnt lgkmcnt(0)
	s_barrier
	s_setprio 1
	s_waitcnt lgkmcnt(6)
	v_mfma_scale_f32_16x16x128_f8f6f4 v[126:129], v[2:9], v[10:17], v[126:129], v172, v172 op_sel:[0,1,0] op_sel_hi:[0,0,0]
	v_mfma_scale_f32_16x16x128_f8f6f4 v[122:125], v[18:25], v[10:17], v[122:125], v172, v172 op_sel:[0,1,0] op_sel_hi:[0,0,0]
	s_waitcnt lgkmcnt(4)
	v_mfma_scale_f32_16x16x128_f8f6f4 v[110:113], v[2:9], v[26:33], v[110:113], v172, v172 op_sel:[0,1,0] op_sel_hi:[0,0,0]
	v_mfma_scale_f32_16x16x128_f8f6f4 v[106:109], v[18:25], v[26:33], v[106:109], v172, v172 op_sel:[0,1,0] op_sel_hi:[0,0,0]
	s_waitcnt lgkmcnt(2)
	v_mfma_scale_f32_16x16x128_f8f6f4 v[94:97], v[2:9], v[34:41], v[208:211], v172, v172 op_sel:[0,1,0] op_sel_hi:[0,0,0]
	v_mfma_scale_f32_16x16x128_f8f6f4 v[90:93], v[18:25], v[34:41], v[212:215], v172, v172 op_sel:[0,1,0] op_sel_hi:[0,0,0]
	s_waitcnt lgkmcnt(0)
	v_mfma_scale_f32_16x16x128_f8f6f4 v[78:81], v[2:9], v[42:49], v[216:219], v172, v172 op_sel:[0,1,0] op_sel_hi:[0,0,0]
	v_mfma_scale_f32_16x16x128_f8f6f4 v[74:77], v[18:25], v[42:49], v[220:223], v172, v172 op_sel:[0,1,0] op_sel_hi:[0,0,0]
	s_setprio 0
	s_setprio 1
	v_mfma_scale_f32_16x16x128_f8f6f4 v[118:121], v[130:137], v[10:17], v[118:121], v172, v172 op_sel:[0,1,0] op_sel_hi:[0,0,0]
	v_mfma_scale_f32_16x16x128_f8f6f4 v[114:117], v[138:145], v[10:17], v[114:117], v172, v172 op_sel:[0,1,0] op_sel_hi:[0,0,0]
	v_mfma_scale_f32_16x16x128_f8f6f4 v[102:105], v[130:137], v[26:33], v[102:105], v172, v172 op_sel:[0,1,0] op_sel_hi:[0,0,0]
	v_mfma_scale_f32_16x16x128_f8f6f4 v[98:101], v[138:145], v[26:33], v[98:101], v172, v172 op_sel:[0,1,0] op_sel_hi:[0,0,0]
	v_mfma_scale_f32_16x16x128_f8f6f4 v[86:89], v[130:137], v[34:41], v[176:179], v172, v172 op_sel:[0,1,0] op_sel_hi:[0,0,0]
	v_mfma_scale_f32_16x16x128_f8f6f4 v[82:85], v[138:145], v[34:41], v[180:183], v172, v172 op_sel:[0,1,0] op_sel_hi:[0,0,0]
	v_mfma_scale_f32_16x16x128_f8f6f4 v[70:73], v[130:137], v[42:49], v[184:187], v172, v172 op_sel:[0,1,0] op_sel_hi:[0,0,0]
	v_mfma_scale_f32_16x16x128_f8f6f4 v[66:69], v[138:145], v[42:49], v[188:191], v172, v172 op_sel:[0,1,0] op_sel_hi:[0,0,0]
	s_setprio 0
	s_barrier
	s_mov_b32 m0, s24
	s_add_i32 s53, s52, 0x80
	ds_read_b128 v[34:37], v171 offset:49152
	ds_read_b128 v[38:41], v171 offset:50176
	ds_read_b128 v[150:153], v171 offset:51200
	ds_read_b128 v[154:157], v171 offset:52224
	ds_read_b128 v[158:161], v171 offset:53248
	ds_read_b128 v[162:165], v171 offset:54272
	ds_read_b128 v[176:179], v171 offset:55296
	ds_read_b128 v[180:183], v171 offset:56320
	buffer_load_dwordx4 v168, s[80:83], s53 offen lds
	s_add_i32 s53, s52, 0x20080
	s_mov_b32 m0, s25
	s_add_i32 s50, s50, 0x20080
	buffer_load_dwordx4 v168, s[80:83], s53 offen lds
	s_add_i32 s53, s52, 0x40080
	s_mov_b32 m0, s28
	s_add_i32 s52, s52, 0x60080
	buffer_load_dwordx4 v168, s[80:83], s53 offen lds
	s_mov_b32 m0, s29
	s_nop 0
	buffer_load_dwordx4 v168, s[80:83], s52 offen lds
	s_mov_b32 m0, s26
	s_nop 0
	buffer_load_dwordx4 v1, s[80:83], s51 offen lds
	s_mov_b32 m0, s27
	s_nop 0
	buffer_load_dwordx4 v1, s[80:83], s50 offen lds
	s_waitcnt vmcnt(8)
	s_waitcnt lgkmcnt(0)
	s_barrier
	s_setprio 1
	s_waitcnt lgkmcnt(6)
	v_mfma_scale_f32_16x16x128_f8f6f4 v[62:65], v[2:9], v[34:41], v[62:65], v172, v172 op_sel:[0,1,0] op_sel_hi:[0,0,0]
	v_mfma_scale_f32_16x16x128_f8f6f4 v[58:61], v[18:25], v[34:41], v[58:61], v172, v172 op_sel:[0,1,0] op_sel_hi:[0,0,0]
	s_waitcnt lgkmcnt(4)
	v_mfma_scale_f32_16x16x128_f8f6f4 v[46:49], v[2:9], v[150:157], v[192:195], v172, v172 op_sel:[0,1,0] op_sel_hi:[0,0,0]
	v_mfma_scale_f32_16x16x128_f8f6f4 v[42:45], v[18:25], v[150:157], v[196:199], v172, v172 op_sel:[0,1,0] op_sel_hi:[0,0,0]
	s_waitcnt lgkmcnt(2)
	v_mfma_scale_f32_16x16x128_f8f6f4 v[30:33], v[2:9], v[158:165], v[200:203], v172, v172 op_sel:[0,1,0] op_sel_hi:[0,0,0]
	v_mfma_scale_f32_16x16x128_f8f6f4 v[26:29], v[18:25], v[158:165], v[204:207], v172, v172 op_sel:[0,1,0] op_sel_hi:[0,0,0]
	s_waitcnt lgkmcnt(0)
	v_mfma_scale_f32_16x16x128_f8f6f4 v[14:17], v[2:9], v[176:183], v[224:227], v172, v172 op_sel:[0,1,0] op_sel_hi:[0,0,0]
	v_mfma_scale_f32_16x16x128_f8f6f4 v[10:13], v[18:25], v[176:183], v[228:231], v172, v172 op_sel:[0,1,0] op_sel_hi:[0,0,0]
	s_setprio 0
	s_setprio 1
	v_mfma_scale_f32_16x16x128_f8f6f4 v[54:57], v[130:137], v[34:41], v[54:57], v172, v172 op_sel:[0,1,0] op_sel_hi:[0,0,0]
	v_mfma_scale_f32_16x16x128_f8f6f4 v[50:53], v[138:145], v[34:41], v[50:53], v172, v172 op_sel:[0,1,0] op_sel_hi:[0,0,0]
	v_mfma_scale_f32_16x16x128_f8f6f4 v[38:41], v[130:137], v[150:157], v[232:235], v172, v172 op_sel:[0,1,0] op_sel_hi:[0,0,0]
	v_mfma_scale_f32_16x16x128_f8f6f4 v[34:37], v[138:145], v[150:157], v[236:239], v172, v172 op_sel:[0,1,0] op_sel_hi:[0,0,0]
	v_mfma_scale_f32_16x16x128_f8f6f4 v[22:25], v[130:137], v[158:165], v[240:243], v172, v172 op_sel:[0,1,0] op_sel_hi:[0,0,0]
	v_mfma_scale_f32_16x16x128_f8f6f4 v[18:21], v[138:145], v[158:165], v[244:247], v172, v172 op_sel:[0,1,0] op_sel_hi:[0,0,0]
	v_mfma_scale_f32_16x16x128_f8f6f4 v[6:9], v[130:137], v[176:183], v[248:251], v172, v172 op_sel:[0,1,0] op_sel_hi:[0,0,0]
	v_mfma_scale_f32_16x16x128_f8f6f4 v[2:5], v[138:145], v[176:183], v[146:149], v172, v172 op_sel:[0,1,0] op_sel_hi:[0,0,0]
	s_setprio 0
	s_barrier
	s_add_i32 s49, s49, 2
	s_addk_i32 s4, 0x100
	s_addk_i32 s5, 0x100
	s_cmp_gt_u32 s49, 13
	s_cbranch_scc0 .LBB0_1725
	s_branch .Lpeel_after_1725
